# P8 conv: pk_mul + 2 adds per tap pair -> 2 fused v_fma_f32 (59 packed multiplies removed per unit); plus DPP wave sums in the row phases
# speedup vs baseline: 1.0071x; 1.0071x over previous
.Lp6_nopf:
	v_and_b32_e32 v83, 0xffff0000, v59
	v_lshlrev_b32_e32 v80, 16, v58
	v_and_b32_e32 v81, 0xffff0000, v58
	v_lshlrev_b32_e32 v82, 16, v59
	v_lshlrev_b32_e32 v67, 16, v52
	v_and_b32_e32 v65, 0xffff0000, v52
	v_lshlrev_b32_e32 v62, 16, v53
	v_and_b32_e32 v63, 0xffff0000, v53
	v_lshlrev_b32_e32 v58, 16, v50
	v_and_b32_e32 v59, 0xffff0000, v50
	v_lshlrev_b32_e32 v60, 16, v51
	v_and_b32_e32 v61, 0xffff0000, v51
	v_lshlrev_b32_e32 v50, 16, v46
	v_and_b32_e32 v51, 0xffff0000, v46
	v_lshlrev_b32_e32 v52, 16, v47
	v_and_b32_e32 v53, 0xffff0000, v47
	v_and_b32_e32 v47, 0xffff0000, v44
	v_mul_f32_e32 v46, v83, v83
	v_and_b32_e32 v87, 0xffff0000, v57
	v_and_b32_e32 v86, 0xffff0000, v56
	v_pk_fma_f32 v[90:91], v[82:83], v[82:83], v[46:47] op_sel_hi:[1,1,0]
	v_mul_f32_e32 v46, v81, v81
	v_lshlrev_b32_e32 v85, 16, v57
	v_lshlrev_b32_e32 v84, 16, v56
	v_pk_mul_f32 v[92:93], v[86:87], v[86:87]
	v_pk_fma_f32 v[94:95], v[80:81], v[80:81], v[46:47] op_sel_hi:[1,1,0]
	v_pk_fma_f32 v[92:93], v[84:85], v[84:85], v[92:93]
	v_mov_b32_e32 v66, v94
	v_mov_b32_e32 v96, v90
	v_mov_b32_e32 v97, v67
	v_lshlrev_b32_e32 v68, 16, v54
	v_and_b32_e32 v69, 0xffff0000, v54
	v_lshlrev_b32_e32 v56, 16, v48
	v_and_b32_e32 v54, 0xffff0000, v48
	v_mul_f32_e32 v48, v65, v65
	v_pk_add_f32 v[90:91], v[94:95], v[90:91]
	v_pk_mul_f32 v[94:95], v[66:67], v[96:97]
	v_pk_add_f32 v[92:93], v[92:93], v[92:93] op_sel:[0,1] op_sel_hi:[1,0]
	v_and_b32_e32 v89, 0xffff0000, v55
	v_mov_b32_e32 v91, v95
	v_mov_b32_e32 v93, v48
	v_mul_f32_e32 v46, v69, v69
	v_lshlrev_b32_e32 v88, 16, v55
	v_pk_add_f32 v[90:91], v[90:91], v[92:93]
	v_pk_fma_f32 v[92:93], v[68:69], v[68:69], v[46:47] op_sel_hi:[1,1,0]
	v_mul_f32_e32 v46, v89, v89
	v_mul_f32_e32 v64, v62, v62
	v_mul_f32_e32 v98, v63, v63
	v_pk_fma_f32 v[94:95], v[88:89], v[88:89], v[46:47] op_sel_hi:[1,1,0]
	v_mov_b32_e32 v93, v64
	v_mov_b32_e32 v95, v98
	v_pk_add_f32 v[92:93], v[92:93], v[94:95]
	v_mul_f32_e32 v46, v61, v61
	v_pk_add_f32 v[90:91], v[90:91], v[92:93]
	v_lshlrev_b32_e32 v57, 16, v49
	v_add_f32_e32 v48, v90, v91
	s_nop 1
	v_add_f32_dpp v237, v48, v48 quad_perm:[1,0,3,2] row_mask:0xf bank_mask:0xf
	s_nop 1
	v_add_f32_dpp v237, v237, v237 quad_perm:[2,3,0,1] row_mask:0xf bank_mask:0xf
	s_nop 1
	v_add_f32_dpp v237, v237, v237 row_half_mirror row_mask:0xf bank_mask:0xf
	s_nop 1
	v_add_f32_dpp v237, v237, v237 row_mirror row_mask:0xf bank_mask:0xf
	s_nop 0
	v_mov_b32_e32 v236, v237
	s_nop 1
	v_permlane16_swap_b32_e32 v237, v236
	s_nop 0
	v_add_f32_e32 v237, v237, v236
	v_mov_b32_e32 v236, v237
	s_nop 1
	v_permlane32_swap_b32_e32 v237, v236
	s_nop 0
	v_add_f32_e32 v237, v237, v236
	v_pk_fma_f32 v[90:91], v[60:61], v[60:61], v[46:47] op_sel_hi:[1,1,0]
	v_mul_f32_e32 v46, v59, v59
	v_pk_fma_f32 v[94:95], v[58:59], v[58:59], v[46:47] op_sel_hi:[1,1,0]
	v_and_b32_e32 v55, 0xffff0000, v49
	s_waitcnt lgkmcnt(0)
	v_lshlrev_b32_e32 v49, 16, v44
	v_mov_b32_e32 v96, v90
	v_mov_b32_e32 v97, v49
	v_pk_add_f32 v[90:91], v[94:95], v[90:91]
	s_waitcnt lgkmcnt(0)
	v_mov_b32_e32 v48, v94
	v_pk_mul_f32 v[94:95], v[48:49], v[96:97]
	v_pk_mul_f32 v[92:93], v[54:55], v[54:55]
	v_mul_f32_e32 v66, v47, v47
	s_waitcnt lgkmcnt(0)
	v_pk_fma_f32 v[92:93], v[56:57], v[56:57], v[92:93]
	v_mov_b32_e32 v91, v95
	v_pk_add_f32 v[92:93], v[92:93], v[92:93] op_sel:[0,1] op_sel_hi:[1,0]
	v_lshlrev_b32_e32 v44, 16, v45
	s_waitcnt lgkmcnt(0)
	v_mov_b32_e32 v93, v66
	v_mul_f32_e32 v46, v51, v51
	v_pk_add_f32 v[90:91], v[90:91], v[92:93]
	v_pk_fma_f32 v[92:93], v[50:51], v[50:51], v[46:47] op_sel_hi:[1,1,0]
	s_waitcnt lgkmcnt(0)
	v_mul_f32_e32 v46, v53, v53
	v_pk_fma_f32 v[94:95], v[52:53], v[52:53], v[46:47] op_sel_hi:[1,1,0]
	v_and_b32_e32 v45, 0xffff0000, v45
	v_mul_f32_e32 v98, v44, v44
	s_waitcnt lgkmcnt(0)
	v_mov_b32_e32 v46, v237
	v_fmamk_f32 v46, v46, 0x3a800000, v79
	v_mul_f32_e32 v48, 0x4b800000, v46
	v_cmp_gt_f32_e32 vcc, s5, v46
	v_mul_f32_e32 v99, v45, v45
	v_mov_b32_e32 v93, v98
	v_cndmask_b32_e32 v46, v46, v48, vcc
	v_rsq_f32_e32 v46, v46
	v_mov_b32_e32 v95, v99
	v_pk_add_f32 v[92:93], v[92:93], v[94:95]
	s_add_i32 s4, s4, 2
	v_pk_add_f32 v[90:91], v[90:91], v[92:93]
	v_mul_f32_e32 v64, 0x45800000, v46
	v_add_f32_e32 v48, v90, v91
	v_cndmask_b32_e32 v46, v46, v64, vcc
	s_nop 1
	v_add_f32_dpp v237, v48, v48 quad_perm:[1,0,3,2] row_mask:0xf bank_mask:0xf
	s_nop 1
	v_add_f32_dpp v237, v237, v237 quad_perm:[2,3,0,1] row_mask:0xf bank_mask:0xf
	s_nop 1
	v_add_f32_dpp v237, v237, v237 row_half_mirror row_mask:0xf bank_mask:0xf
	s_nop 1
	v_add_f32_dpp v237, v237, v237 row_mirror row_mask:0xf bank_mask:0xf
	s_nop 0
	v_mov_b32_e32 v236, v237
	s_nop 1
	v_permlane16_swap_b32_e32 v237, v236
	s_nop 0
	v_add_f32_e32 v237, v237, v236
	v_mov_b32_e32 v236, v237
	s_nop 1
	v_permlane32_swap_b32_e32 v237, v236
	s_nop 0
	v_add_f32_e32 v237, v237, v236
	v_pk_mul_f32 v[80:81], v[46:47], v[80:81] op_sel_hi:[0,1]
	v_pk_mul_f32 v[82:83], v[46:47], v[82:83] op_sel_hi:[0,1]
	v_pk_fma_f32 v[80:81], v[18:19], v[80:81], v[2:3]
	v_pk_fma_f32 v[82:83], v[20:21], v[82:83], v[4:5]
	s_waitcnt lgkmcnt(0)
	v_cvt_pk_bf16_f32 v80, v80, v81
	v_cvt_pk_bf16_f32 v81, v82, v83
	global_store_dwordx2 v[42:43], v[80:81], off offset:-3584
	v_mov_b32_e32 v80, v84
	s_waitcnt lgkmcnt(0)
	v_mov_b32_e32 v81, v86
	v_pk_mul_f32 v[80:81], v[46:47], v[80:81] op_sel_hi:[0,1]
	v_mov_b32_e32 v86, v85
	v_pk_mul_f32 v[82:83], v[46:47], v[86:87] op_sel_hi:[0,1]
	s_waitcnt lgkmcnt(0)
	v_pk_fma_f32 v[80:81], v[22:23], v[80:81], v[6:7]
	v_pk_fma_f32 v[82:83], v[24:25], v[82:83], v[8:9]
	v_cvt_pk_bf16_f32 v80, v80, v81
	v_pk_mul_f32 v[68:69], v[46:47], v[68:69] op_sel_hi:[0,1]
	s_waitcnt lgkmcnt(0)
	v_cvt_pk_bf16_f32 v81, v82, v83
	v_mov_b32_e32 v64, v67
	global_store_dwordx2 v[42:43], v[80:81], off offset:-3072
	v_pk_mul_f32 v[80:81], v[46:47], v[88:89] op_sel_hi:[0,1]
	s_waitcnt lgkmcnt(0)
	v_pk_mul_f32 v[64:65], v[46:47], v[64:65] op_sel_hi:[0,1]
	v_pk_mul_f32 v[62:63], v[46:47], v[62:63] op_sel_hi:[0,1]
	v_pk_fma_f32 v[68:69], v[26:27], v[68:69], v[10:11]
	v_pk_fma_f32 v[64:65], v[30:31], v[64:65], v[14:15]
	s_waitcnt lgkmcnt(0)
	v_mov_b32_e32 v46, v237
	v_fmamk_f32 v46, v46, 0x3a800000, v79
	v_mul_f32_e32 v48, 0x4b800000, v46
	v_cmp_gt_f32_e32 vcc, s5, v46
	v_pk_fma_f32 v[80:81], v[28:29], v[80:81], v[12:13]
	v_cvt_pk_bf16_f32 v68, v68, v69
	v_pk_fma_f32 v[62:63], v[32:33], v[62:63], v[16:17]
	v_cndmask_b32_e32 v46, v46, v48, vcc
	v_rsq_f32_e32 v46, v46
	v_cvt_pk_bf16_f32 v69, v80, v81
	global_store_dwordx2 v[42:43], v[68:69], off offset:-2560
	v_cvt_pk_bf16_f32 v64, v64, v65
	v_mul_f32_e32 v48, 0x45800000, v46
	v_cndmask_b32_e32 v48, v46, v48, vcc
	v_pk_mul_f32 v[58:59], v[48:49], v[58:59] op_sel_hi:[0,1]
	v_pk_mul_f32 v[60:61], v[48:49], v[60:61] op_sel_hi:[0,1]
	v_pk_fma_f32 v[58:59], v[18:19], v[58:59], v[2:3]
	v_cvt_pk_bf16_f32 v65, v62, v63
	global_store_dwordx2 v[42:43], v[64:65], off offset:-2048
	v_pk_fma_f32 v[60:61], v[20:21], v[60:61], v[4:5]
	v_cvt_pk_bf16_f32 v58, v58, v59
	v_mov_b32_e32 v46, v49
	v_cvt_pk_bf16_f32 v59, v60, v61
	global_store_dwordx2 v[42:43], v[58:59], off offset:-1536
	v_mov_b32_e32 v58, v56
	v_mov_b32_e32 v59, v54
	v_pk_mul_f32 v[58:59], v[48:49], v[58:59] op_sel_hi:[0,1]
	v_mov_b32_e32 v54, v57
	v_pk_mul_f32 v[50:51], v[48:49], v[50:51] op_sel_hi:[0,1]
	v_pk_mul_f32 v[46:47], v[48:49], v[46:47] op_sel_hi:[0,1]
	v_pk_mul_f32 v[54:55], v[48:49], v[54:55] op_sel_hi:[0,1]
	v_pk_fma_f32 v[56:57], v[22:23], v[58:59], v[6:7]
	v_pk_mul_f32 v[52:53], v[48:49], v[52:53] op_sel_hi:[0,1]
	v_pk_fma_f32 v[50:51], v[26:27], v[50:51], v[10:11]
	v_pk_mul_f32 v[44:45], v[48:49], v[44:45] op_sel_hi:[0,1]
	v_pk_fma_f32 v[46:47], v[30:31], v[46:47], v[14:15]
	v_pk_fma_f32 v[54:55], v[24:25], v[54:55], v[8:9]
	v_cvt_pk_bf16_f32 v56, v56, v57
	v_pk_fma_f32 v[52:53], v[28:29], v[52:53], v[12:13]
	v_cvt_pk_bf16_f32 v57, v54, v55
	global_store_dwordx2 v[42:43], v[56:57], off offset:-1024
	v_cvt_pk_bf16_f32 v50, v50, v51
	v_cvt_pk_bf16_f32 v51, v52, v53
	global_store_dwordx2 v[42:43], v[50:51], off offset:-512
	v_pk_fma_f32 v[44:45], v[32:33], v[44:45], v[16:17]
	v_cvt_pk_bf16_f32 v46, v46, v47
	s_cmp_lt_i32 s4, s3
	v_cvt_pk_bf16_f32 v47, v44, v45
	global_store_dwordx2 v[42:43], v[46:47], off
	v_lshl_add_u64 v[42:43], v[42:43], 0, s[6:7]
	s_cbranch_scc0 .LBB0_1014
	s_ashr_i32 s9, s4, 31
	s_branch .Lp6_chk

.LBB0_1262:
	s_mul_hi_i32 s20, s80, 0x66666667
	s_lshr_b32 s48, s20, 31
	s_ashr_i32 s20, s20, 2
	s_add_i32 s20, s20, s48
	s_mul_i32 s48, s20, 0xfffffb00
	s_add_i32 s48, s48, s35
	s_waitcnt lgkmcnt(0)
	v_add_u32_e32 v2, s48, v158
	v_ashrrev_i32_e32 v3, 31, v2
	v_lshlrev_b64 v[2:3], 2, v[2:3]
	v_lshl_add_u64 v[6:7], s[62:63], 0, v[2:3]
	v_add_co_u32_e32 v4, vcc, s3, v6
	global_load_dwordx4 v[58:61], v[6:7], off
	s_nop 0
	v_addc_co_u32_e32 v5, vcc, 0, v7, vcc
	global_load_dwordx4 v[94:97], v[4:5], off offset:1024
	v_lshl_add_u64 v[2:3], s[64:65], 0, v[2:3]
	global_load_dwordx4 v[70:73], v[2:3], off
	v_lshl_add_u64 v[4:5], v[6:7], 0, s[38:39]
	global_load_dwordx4 v[98:101], v[4:5], off offset:16
	global_load_dwordx4 v[62:65], v[6:7], off offset:16
	global_load_dwordx4 v[66:69], v[2:3], off offset:16
	s_mul_i32 s52, s20, 0xffffffec
	v_add_co_u32_e32 v2, vcc, s29, v6
	s_add_i32 s52, s33, s52
	s_nop 0
	v_addc_co_u32_e32 v3, vcc, 0, v7, vcc
	s_ashr_i32 s53, s52, 31
	v_add_co_u32_e32 v4, vcc, s47, v6
	s_lshl_b64 s[54:55], s[52:53], 16
	s_nop 0
	v_addc_co_u32_e32 v5, vcc, 0, v7, vcc
	v_lshl_add_u64 v[8:9], v[156:157], 0, s[54:55]
	global_load_dwordx4 v[102:105], v[4:5], off offset:3072
	global_load_dwordx4 v[86:89], v[2:3], off offset:2048
	global_load_dwordx4 v[42:45], v[8:9], off
	global_load_dwordx4 v[26:29], v[8:9], off offset:1024
	global_load_dwordx4 v[10:13], v[8:9], off offset:2048
	s_nop 0
	global_load_dwordx4 v[2:5], v[8:9], off offset:3072
	v_add_co_u32_e32 v22, vcc, s3, v8
	v_lshlrev_b32_e32 v111, 16, v201
	s_nop 0
	v_addc_co_u32_e32 v23, vcc, 0, v9, vcc
	v_add_co_u32_e32 v24, vcc, s29, v8
	v_lshlrev_b32_e32 v110, 16, v206
	s_nop 0
	v_addc_co_u32_e32 v25, vcc, 0, v9, vcc
	s_waitcnt vmcnt(0)
	v_add_co_u32_e32 v82, vcc, s47, v8
	global_load_dwordx4 v[30:33], v[22:23], off offset:1024
	global_load_dwordx4 v[14:17], v[22:23], off offset:2048
	global_load_dwordx4 v[46:49], v[24:25], off offset:-4096
	global_load_dwordx4 v[50:53], v[24:25], off
	global_load_dwordx4 v[34:37], v[24:25], off offset:1024
	global_load_dwordx4 v[18:21], v[24:25], off offset:2048
	v_addc_co_u32_e32 v83, vcc, 0, v9, vcc
	v_lshl_add_u64 v[8:9], v[6:7], 0, s[40:41]
	v_lshl_add_u64 v[6:7], v[6:7], 0, s[42:43]
	global_load_dwordx4 v[106:109], v[6:7], off offset:16
	global_load_dwordx4 v[74:77], v[8:9], off offset:16
	global_load_dwordx4 v[78:81], v[24:25], off offset:3072
	s_nop 0
	global_load_dwordx4 v[6:9], v[22:23], off offset:3072
	global_load_dwordx4 v[54:57], v[82:83], off
	global_load_dwordx4 v[38:41], v[82:83], off offset:1024
	s_nop 0
	global_load_dwordx4 v[22:25], v[82:83], off offset:2048
	s_nop 0
	global_load_dwordx4 v[82:85], v[82:83], off offset:3072
	v_lshlrev_b32_e32 v114, 16, v207
	v_lshlrev_b32_e32 v115, 16, v202
	v_and_b32_e32 v117, 0xffff0000, v202
	v_and_b32_e32 v116, 0xffff0000, v207
	v_and_b32_e32 v113, 0xffff0000, v201
	v_and_b32_e32 v112, 0xffff0000, v206
	v_and_b32_e32 v121, 0xffff0000, v203
	v_and_b32_e32 v120, 0xffff0000, v209
	v_lshlrev_b32_e32 v122, 16, v210
	v_lshlrev_b32_e32 v123, 16, v205
	v_and_b32_e32 v125, 0xffff0000, v205
	v_and_b32_e32 v124, 0xffff0000, v210
	v_lshlrev_b32_e32 v127, 16, v212
	v_lshlrev_b32_e32 v126, 16, v218
	v_and_b32_e32 v129, 0xffff0000, v212
	v_and_b32_e32 v128, 0xffff0000, v218
	v_lshlrev_b32_e32 v131, 16, v213
	v_and_b32_e32 v133, 0xffff0000, v213
	v_and_b32_e32 v132, 0xffff0000, v219
	v_lshlrev_b32_e32 v135, 16, v215
	v_and_b32_e32 v137, 0xffff0000, v215
	v_and_b32_e32 v136, 0xffff0000, v221
	v_lshlrev_b32_e32 v139, 16, v216
	v_and_b32_e32 v141, 0xffff0000, v216
	v_and_b32_e32 v140, 0xffff0000, v222
	s_and_b32 s49, s79, 0x8000
	s_add_i32 s49, s49, 0
	v_add3_u32 v147, s49, v186, v187
	s_add_i32 s53, s31, s49
	s_add_i32 s52, s52, 1
	v_add_u32_e32 v245, s49, v165
	v_mov_b32_e32 v93, v58
	v_mov_b32_e32 v91, v60
	v_mov_b32_e32 v92, v94
	v_mov_b32_e32 v58, v95
	v_mov_b32_e32 v90, v96
	v_mov_b32_e32 v60, v97
	v_fma_f32 v95, v93, v111, v70
	v_pk_mul_f32 v[118:119], v[90:91], v[114:115]
	v_fma_f32 v115, v92, v110, v95
	v_add_f32_e32 v111, v119, v72
	v_fma_f32 v95, v61, v117, v73
	v_fma_f32 v97, v59, v113, v71
	v_add_f32_e32 v111, v118, v111
	v_fma_f32 v134, v60, v116, v95
	v_lshlrev_b32_e32 v119, 16, v203
	v_lshlrev_b32_e32 v118, 16, v209
	v_mov_b32_e32 v94, v98
	v_mov_b32_e32 v95, v62
	v_fma_f32 v130, v58, v112, v97
	s_nop 0
	v_fma_f32 v62, v95, v119, v66
	v_fma_f32 v119, v94, v118, v62
	v_mov_b32_e32 v62, v99
	s_nop 0
	v_fma_f32 v97, v63, v121, v67
	v_fma_f32 v138, v62, v120, v97
	v_mov_b32_e32 v96, v100
	v_mov_b32_e32 v97, v64
	s_nop 0
	v_fma_f32 v64, v97, v123, v68
	v_fma_f32 v123, v96, v122, v64
	v_mov_b32_e32 v64, v101
	s_nop 0
	v_fma_f32 v99, v65, v125, v69
	v_fma_f32 v142, v64, v124, v99
	v_mov_b32_e32 v98, v102
	v_mov_b32_e32 v99, v86
	s_nop 0
	v_fma_f32 v86, v99, v127, v115
	v_fma_f32 v115, v98, v126, v86
	v_mov_b32_e32 v86, v103
	s_nop 0
	v_fma_f32 v101, v87, v129, v130
	v_fma_f32 v143, v86, v128, v101
	v_lshlrev_b32_e32 v130, 16, v219
	v_mov_b32_e32 v100, v104
	v_mov_b32_e32 v101, v88
	s_nop 0
	v_fma_f32 v88, v101, v131, v111
	v_fma_f32 v111, v100, v130, v88
	v_mov_b32_e32 v88, v105
	s_nop 0
	v_fma_f32 v103, v89, v133, v134
	v_fma_f32 v144, v88, v132, v103
	v_lshlrev_b32_e32 v134, 16, v221
	s_waitcnt vmcnt(7)
	v_mov_b32_e32 v102, v106
	s_waitcnt vmcnt(6)
	v_mov_b32_e32 v103, v74
	s_nop 0
	v_fma_f32 v74, v103, v135, v119
	v_fma_f32 v119, v102, v134, v74
	v_mov_b32_e32 v74, v107
	s_nop 0
	v_fma_f32 v105, v75, v137, v138
	v_fma_f32 v145, v74, v136, v105
	v_lshlrev_b32_e32 v138, 16, v222
	v_mov_b32_e32 v104, v108
	v_mov_b32_e32 v105, v76
	s_nop 0
	v_fma_f32 v76, v105, v139, v123
	v_fma_f32 v123, v104, v138, v76
	v_mov_b32_e32 v76, v109
	s_nop 0
	v_fma_f32 v107, v77, v141, v142
	v_fma_f32 v109, v76, v140, v107
	v_cvt_pk_bf16_f32 v106, v115, v143
	v_cvt_pk_bf16_f32 v107, v111, v144
	v_add3_u32 v111, s49, v184, v185
	v_cvt_pk_bf16_f32 v108, v119, v145
	v_cvt_pk_bf16_f32 v109, v123, v109
	ds_write_b128 v111, v[106:109]
	v_pk_mov_b32 v[106:107], v[126:127], v[110:111] op_sel:[1,0]
	v_lshlrev_b32_e32 v111, 16, v224
	v_lshlrev_b32_e32 v110, 16, v228
	v_fma_f32 v107, v93, v107, v70
	v_fma_f32 v108, v92, v106, v107
	v_pk_mov_b32 v[106:107], v[128:129], v[112:113] op_sel:[1,0]
	v_pk_mov_b32 v[112:113], v[110:111], v[126:127] op_sel:[1,0]
	s_nop 0
	v_fma_f32 v107, v59, v107, v71
	v_fma_f32 v109, v58, v106, v107
	v_pk_mov_b32 v[106:107], v[130:131], v[114:115] op_sel:[1,0]
	v_and_b32_e32 v115, 0xffff0000, v224
	s_nop 0
	v_fma_f32 v107, v91, v107, v72
	v_fma_f32 v123, v90, v106, v107
	v_pk_mov_b32 v[106:107], v[132:133], v[116:117] op_sel:[1,0]
	s_nop 0
	s_nop 0
	v_fma_f32 v107, v61, v107, v73
	v_fma_f32 v142, v60, v106, v107
	v_pk_mov_b32 v[106:107], v[134:135], v[118:119] op_sel:[1,0]
	s_nop 0
	s_nop 0
	v_fma_f32 v107, v95, v107, v66
	v_fma_f32 v143, v94, v106, v107
	v_pk_mov_b32 v[106:107], v[136:137], v[120:121] op_sel:[1,0]
	s_nop 0
	s_nop 0
	v_fma_f32 v107, v63, v107, v67
	v_fma_f32 v144, v62, v106, v107
	v_pk_mov_b32 v[106:107], v[138:139], v[122:123] op_sel:[1,0]
	s_nop 0
	s_nop 0
	v_fma_f32 v107, v97, v107, v68
	v_fma_f32 v145, v96, v106, v107
	v_pk_mov_b32 v[106:107], v[140:141], v[124:125] op_sel:[1,0]
	s_nop 0
	s_nop 0
	v_fma_f32 v107, v65, v107, v69
	v_fma_f32 v146, v64, v106, v107
	v_pk_mul_f32 v[106:107], v[92:93], v[126:127]
	v_lshlrev_b32_e32 v127, 16, v226
	v_add_f32_e32 v107, v107, v70
	v_add_f32_e32 v114, v106, v107
	v_pk_mul_f32 v[92:93], v[92:93], v[112:113]
	v_fma_f32 v107, v59, v129, v71
	v_fma_f32 v118, v58, v128, v107
	v_add_f32_e32 v70, v93, v70
	v_fma_f32 v107, v91, v131, v72
	v_fma_f32 v122, v90, v130, v107
	v_add_f32_e32 v70, v92, v70
	v_fma_f32 v107, v61, v133, v73
	v_fma_f32 v148, v60, v132, v107
	s_nop 0
	v_fma_f32 v107, v95, v135, v66
	v_fma_f32 v149, v94, v134, v107
	s_nop 0
	v_fma_f32 v107, v63, v137, v67
	v_fma_f32 v150, v62, v136, v107
	s_nop 0
	v_fma_f32 v107, v97, v139, v68
	v_fma_f32 v151, v96, v138, v107
	s_nop 0
	v_fma_f32 v107, v65, v141, v69
	v_fma_f32 v152, v64, v140, v107
	s_nop 0
	v_fma_f32 v107, v99, v113, v108
	v_fma_f32 v119, v98, v112, v107
	s_nop 0
	v_fma_f32 v107, v99, v111, v114
	v_and_b32_e32 v114, 0xffff0000, v228
	v_pk_mov_b32 v[116:117], v[114:115], v[128:129] op_sel:[1,0]
	v_fma_f32 v111, v98, v110, v107
	v_pk_mul_f32 v[58:59], v[58:59], v[116:117]
	v_fma_f32 v107, v87, v117, v109
	v_fma_f32 v106, v86, v116, v107
	v_cvt_pk_bf16_f32 v106, v119, v106
	v_lshlrev_b32_e32 v119, 16, v225
	v_fma_f32 v107, v87, v115, v118
	v_lshlrev_b32_e32 v118, 16, v229
	v_pk_mov_b32 v[120:121], v[118:119], v[130:131] op_sel:[1,0]
	v_fma_f32 v115, v86, v114, v107
	v_and_b32_e32 v131, 0xffff0000, v226
	v_fma_f32 v107, v101, v121, v123
	v_fma_f32 v107, v100, v120, v107
	v_and_b32_e32 v123, 0xffff0000, v225
	v_fma_f32 v109, v101, v119, v122
	v_and_b32_e32 v122, 0xffff0000, v229
	v_pk_mov_b32 v[124:125], v[122:123], v[132:133] op_sel:[1,0]
	v_fma_f32 v119, v100, v118, v109
	v_and_b32_e32 v130, 0xffff0000, v230
	v_fma_f32 v109, v89, v125, v142
	v_fma_f32 v126, v88, v124, v109
	v_cvt_pk_bf16_f32 v107, v107, v126
	v_lshlrev_b32_e32 v126, 16, v230
	v_fma_f32 v109, v89, v123, v148
	v_pk_mov_b32 v[128:129], v[126:127], v[134:135] op_sel:[1,0]
	v_fma_f32 v123, v88, v122, v109
	v_pk_mov_b32 v[132:133], v[130:131], v[136:137] op_sel:[1,0]
	v_fma_f32 v109, v103, v129, v143
	v_fma_f32 v142, v102, v128, v109
	v_add_f32_e32 v59, v59, v71
	v_fma_f32 v109, v103, v127, v149
	v_fma_f32 v127, v102, v126, v109
	v_fma_f32 v109, v75, v133, v144
	v_add_f32_e32 v71, v58, v59
	v_fma_f32 v108, v74, v132, v109
	v_fma_f32 v109, v75, v131, v150
	v_fma_f32 v59, v91, v121, v72
	v_fma_f32 v131, v74, v130, v109
	v_lshlrev_b32_e32 v134, 16, v231
	v_lshlrev_b32_e32 v135, 16, v227
	v_fma_f32 v72, v90, v120, v59
	v_pk_mov_b32 v[136:137], v[134:135], v[138:139] op_sel:[1,0]
	v_fma_f32 v59, v61, v125, v73
	v_fma_f32 v60, v60, v124, v59
	v_fma_f32 v109, v105, v137, v145
	v_fma_f32 v59, v95, v129, v66
	v_fma_f32 v109, v104, v136, v109
	v_fma_f32 v61, v94, v128, v59
	v_fma_f32 v135, v105, v135, v151
	v_fma_f32 v59, v63, v133, v67
	v_fma_f32 v135, v104, v134, v135
	v_and_b32_e32 v139, 0xffff0000, v227
	v_and_b32_e32 v138, 0xffff0000, v231
	v_fma_f32 v62, v62, v132, v59
	v_pk_mov_b32 v[140:141], v[138:139], v[140:141] op_sel:[1,0]
	v_fma_f32 v59, v97, v137, v68
	v_fma_f32 v63, v96, v136, v59
	v_cvt_pk_bf16_f32 v108, v142, v108
	v_fma_f32 v59, v65, v141, v69
	v_fma_f32 v64, v64, v140, v59
	v_lshlrev_b32_e32 v58, 16, v232
	v_mov_b32_e32 v59, v110
	v_fma_f32 v143, v77, v141, v146
	v_fma_f32 v59, v99, v59, v70
	v_fma_f32 v65, v98, v58, v59
	v_and_b32_e32 v58, 0xffff0000, v232
	v_mov_b32_e32 v59, v114
	v_fma_f32 v144, v76, v140, v143
	v_fma_f32 v59, v87, v59, v71
	v_fma_f32 v66, v86, v58, v59
	v_lshlrev_b32_e32 v58, 16, v233
	v_mov_b32_e32 v59, v118
	v_pk_mul_f32 v[142:143], v[76:77], v[138:139]
	v_fma_f32 v59, v101, v59, v72
	v_fma_f32 v67, v100, v58, v59
	v_and_b32_e32 v58, 0xffff0000, v233
	v_mov_b32_e32 v59, v122
	v_add_f32_e32 v139, v143, v152
	v_fma_f32 v59, v89, v59, v60
	v_fma_f32 v60, v88, v58, v59
	v_lshlrev_b32_e32 v58, 16, v234
	v_mov_b32_e32 v59, v126
	v_cvt_pk_bf16_f32 v109, v109, v144
	ds_write_b128 v147, v[106:109]
	v_fma_f32 v59, v103, v59, v61
	v_fma_f32 v61, v102, v58, v59
	v_and_b32_e32 v58, 0xffff0000, v234
	v_mov_b32_e32 v59, v130
	v_add_f32_e32 v109, v142, v139
	v_fma_f32 v59, v75, v59, v62
	v_fma_f32 v62, v74, v58, v59
	v_lshlrev_b32_e32 v58, 16, v235
	v_mov_b32_e32 v59, v134
	v_cvt_pk_bf16_f32 v106, v111, v115
	v_add3_u32 v111, s49, v188, v189
	v_fma_f32 v59, v105, v59, v63
	v_fma_f32 v63, v104, v58, v59
	v_and_b32_e32 v58, 0xffff0000, v235
	v_mov_b32_e32 v59, v138
	v_cvt_pk_bf16_f32 v107, v119, v123
	v_cvt_pk_bf16_f32 v108, v127, v131
	v_cvt_pk_bf16_f32 v109, v135, v109
	ds_write_b128 v111, v[106:109]
	v_fma_f32 v59, v77, v59, v64
	v_fma_f32 v64, v76, v58, v59
	v_cvt_pk_bf16_f32 v58, v65, v66
	v_cvt_pk_bf16_f32 v59, v67, v60
	v_cvt_pk_bf16_f32 v60, v61, v62
	v_add3_u32 v62, s49, v190, v191
	v_cvt_pk_bf16_f32 v61, v63, v64
	ds_write_b128 v62, v[58:61]
	v_add_u32_e32 v58, s53, v192
	v_add_u32_e32 v242, v58, v193
	s_waitcnt lgkmcnt(0)
	s_barrier
	ds_read_b128 v[58:61], v242
	ds_read_b128 v[62:65], v242 offset:4096
	ds_read_b128 v[98:101], v242 offset:8192
	ds_read_b128 v[102:105], v242 offset:12288
	s_waitcnt lgkmcnt(3)
	v_mfma_f32_16x16x32_bf16 v[66:69], v[42:45], v[58:61], 0
	v_mfma_f32_16x16x32_bf16 v[70:73], v[46:49], v[58:61], 0
	v_mfma_f32_16x16x32_bf16 v[74:77], v[50:53], v[58:61], 0
	s_waitcnt vmcnt(3)
	v_mfma_f32_16x16x32_bf16 v[58:61], v[54:57], v[58:61], 0
	s_waitcnt lgkmcnt(2)
	v_mfma_f32_16x16x32_bf16 v[86:89], v[42:45], v[62:65], 0
	v_mfma_f32_16x16x32_bf16 v[90:93], v[46:49], v[62:65], 0
	v_mfma_f32_16x16x32_bf16 v[94:97], v[50:53], v[62:65], 0
	v_mfma_f32_16x16x32_bf16 v[62:65], v[54:57], v[62:65], 0
	s_waitcnt lgkmcnt(1)
	v_mfma_f32_16x16x32_bf16 v[106:109], v[42:45], v[98:101], 0
	v_mfma_f32_16x16x32_bf16 v[110:113], v[46:49], v[98:101], 0
	v_mfma_f32_16x16x32_bf16 v[114:117], v[50:53], v[98:101], 0
	v_mfma_f32_16x16x32_bf16 v[98:101], v[54:57], v[98:101], 0
	s_waitcnt lgkmcnt(0)
	v_mfma_f32_16x16x32_bf16 v[42:45], v[42:45], v[102:105], 0
	v_mfma_f32_16x16x32_bf16 v[46:49], v[46:49], v[102:105], 0
	v_mfma_f32_16x16x32_bf16 v[50:53], v[50:53], v[102:105], 0
	v_mfma_f32_16x16x32_bf16 v[54:57], v[54:57], v[102:105], 0
	v_add_u32_e32 v102, s53, v194
	v_add_u32_e32 v243, v102, v193
	ds_read_b128 v[102:105], v243
	ds_read_b128 v[118:121], v243 offset:4096
	s_waitcnt lgkmcnt(1)
	v_mfma_f32_16x16x32_bf16 v[66:69], v[26:29], v[102:105], v[66:69]
	v_mfma_f32_16x16x32_bf16 v[70:73], v[30:33], v[102:105], v[70:73]
	v_mfma_f32_16x16x32_bf16 v[74:77], v[34:37], v[102:105], v[74:77]
	s_waitcnt vmcnt(2)
	v_mfma_f32_16x16x32_bf16 v[58:61], v[38:41], v[102:105], v[58:61]
	s_waitcnt lgkmcnt(0)
	v_mfma_f32_16x16x32_bf16 v[86:89], v[26:29], v[118:121], v[86:89]
	v_mfma_f32_16x16x32_bf16 v[90:93], v[30:33], v[118:121], v[90:93]
	v_mfma_f32_16x16x32_bf16 v[94:97], v[34:37], v[118:121], v[94:97]
	v_mfma_f32_16x16x32_bf16 v[62:65], v[38:41], v[118:121], v[62:65]
	ds_read_b128 v[102:105], v243 offset:8192
	ds_read_b128 v[118:121], v243 offset:12288
	s_waitcnt lgkmcnt(1)
	v_mfma_f32_16x16x32_bf16 v[106:109], v[26:29], v[102:105], v[106:109]
	s_waitcnt lgkmcnt(0)
	v_mfma_f32_16x16x32_bf16 v[26:29], v[26:29], v[118:121], v[42:45]
	s_nop 2
	v_add_u32_e32 v42, s53, v195
	v_add_u32_e32 v244, v42, v193
	v_mfma_f32_16x16x32_bf16 v[110:113], v[30:33], v[102:105], v[110:113]
	v_mfma_f32_16x16x32_bf16 v[30:33], v[30:33], v[118:121], v[46:49]
	ds_read_b128 v[42:45], v244
	s_nop 1
	ds_read_b128 v[46:49], v244 offset:4096
	v_mfma_f32_16x16x32_bf16 v[114:117], v[34:37], v[102:105], v[114:117]
	v_mfma_f32_16x16x32_bf16 v[98:101], v[38:41], v[102:105], v[98:101]
	v_mfma_f32_16x16x32_bf16 v[34:37], v[34:37], v[118:121], v[50:53]
	v_mfma_f32_16x16x32_bf16 v[38:41], v[38:41], v[118:121], v[54:57]
	s_waitcnt lgkmcnt(1)
	v_mfma_f32_16x16x32_bf16 v[50:53], v[10:13], v[42:45], v[66:69]
	v_mfma_f32_16x16x32_bf16 v[54:57], v[14:17], v[42:45], v[70:73]
	v_mfma_f32_16x16x32_bf16 v[66:69], v[18:21], v[42:45], v[74:77]
	s_waitcnt vmcnt(1)
	v_mfma_f32_16x16x32_bf16 v[42:45], v[22:25], v[42:45], v[58:61]
	s_waitcnt lgkmcnt(0)
	v_mfma_f32_16x16x32_bf16 v[58:61], v[10:13], v[46:49], v[86:89]
	v_mfma_f32_16x16x32_bf16 v[70:73], v[14:17], v[46:49], v[90:93]
	v_mfma_f32_16x16x32_bf16 v[74:77], v[18:21], v[46:49], v[94:97]
	v_mfma_f32_16x16x32_bf16 v[46:49], v[22:25], v[46:49], v[62:65]
	s_nop 2
	ds_read_b128 v[62:65], v244 offset:8192
	ds_read_b128 v[86:89], v244 offset:12288
	s_waitcnt lgkmcnt(1)
	v_mfma_f32_16x16x32_bf16 v[114:117], v[18:21], v[62:65], v[114:117]
	s_waitcnt lgkmcnt(0)
	v_mfma_f32_16x16x32_bf16 v[176:179], v[18:21], v[86:89], v[34:37]
	v_add_u32_e32 v18, s53, v196
	v_add_u32_e32 v241, v18, v193
	s_ashr_i32 s53, s52, 31
	v_mfma_f32_16x16x32_bf16 v[90:93], v[10:13], v[62:65], v[106:109]
	s_lshl_b64 s[52:53], s[52:53], 16
	v_mfma_f32_16x16x32_bf16 v[110:113], v[14:17], v[62:65], v[110:113]
	v_mfma_f32_16x16x32_bf16 v[62:65], v[22:25], v[62:65], v[98:101]
	v_mfma_f32_16x16x32_bf16 v[180:183], v[22:25], v[86:89], v[38:41]
	ds_read_b128 v[18:21], v241
	ds_read_b128 v[22:25], v241 offset:4096
	s_waitcnt lgkmcnt(1)
	v_mfma_f32_16x16x32_bf16 v[150:153], v[2:5], v[18:21], v[50:53]
	v_mfma_f32_16x16x32_bf16 v[146:149], v[6:9], v[18:21], v[54:57]
	v_mfma_f32_16x16x32_bf16 v[106:109], v[78:81], v[18:21], v[66:69]
	s_waitcnt vmcnt(0)
	v_mfma_f32_16x16x32_bf16 v[102:105], v[82:85], v[18:21], v[42:45]
	ds_read_b128 v[18:21], v241 offset:8192
	ds_read_b128 v[246:249], v241 offset:12288
	s_waitcnt lgkmcnt(2)
	v_mfma_f32_16x16x32_bf16 v[142:145], v[2:5], v[22:25], v[58:61]
	v_mfma_f32_16x16x32_bf16 v[138:141], v[6:9], v[22:25], v[70:73]
	v_mfma_f32_16x16x32_bf16 v[98:101], v[78:81], v[22:25], v[74:77]
	v_mfma_f32_16x16x32_bf16 v[94:97], v[82:85], v[22:25], v[46:49]
	v_add_u32_e32 v22, s48, v159
	v_ashrrev_i32_e32 v23, 31, v22
	v_lshlrev_b64 v[24:25], 2, v[22:23]
	v_lshl_add_u64 v[174:175], s[12:13], 0, v[24:25]
	s_waitcnt lgkmcnt(1)
	v_mfma_f32_16x16x32_bf16 v[134:137], v[2:5], v[18:21], v[90:93]
	v_lshl_add_u64 v[172:173], s[16:17], 0, v[24:25]
	v_add_u32_e32 v22, 16, v22
	v_ashrrev_i32_e32 v23, 31, v22
	v_mfma_f32_16x16x32_bf16 v[90:93], v[78:81], v[18:21], v[114:117]
	global_load_dwordx4 v[118:121], v[174:175], off
	global_load_dwordx4 v[74:77], v[174:175], off offset:64
	s_nop 0
	global_load_dwordx4 v[114:117], v[172:173], off
	global_load_dwordx4 v[70:73], v[172:173], off offset:64
	v_lshl_add_u64 v[168:169], s[18:19], 0, v[24:25]
	s_waitcnt vmcnt(3)
	v_pk_add_f32 v[150:151], v[118:119], v[150:151]
	v_mfma_f32_16x16x32_bf16 v[10:13], v[10:13], v[86:89], v[26:29]
	s_waitcnt vmcnt(1)
	v_pk_add_f32 v[146:147], v[114:115], v[146:147]
	v_pk_mul_f32 v[150:151], v[150:151], s[44:45] op_sel_hi:[1,0]
	v_pk_mul_f32 v[146:147], v[146:147], s[44:45] op_sel_hi:[1,0]
	v_mfma_f32_16x16x32_bf16 v[14:17], v[14:17], v[86:89], v[30:33]
	v_exp_f32_e32 v150, v150
	v_exp_f32_e32 v151, v151
	s_waitcnt lgkmcnt(0)
	v_mfma_f32_16x16x32_bf16 v[126:129], v[2:5], v[246:249], v[10:13]
	v_lshl_add_u64 v[2:3], v[22:23], 2, s[18:19]
	s_nop 1
	v_lshl_add_u64 v[10:11], v[156:157], 0, s[52:53]
	v_add_co_u32_e32 v12, vcc, s3, v10
	v_mfma_f32_16x16x32_bf16 v[130:133], v[6:9], v[18:21], v[110:113]
	s_nop 0
	v_addc_co_u32_e32 v13, vcc, 0, v11, vcc
	s_nop 0
	global_load_dwordx4 v[110:113], v[168:169], off
	global_load_dwordx4 v[66:69], v[2:3], off
	v_mfma_f32_16x16x32_bf16 v[122:125], v[6:9], v[246:249], v[14:17]
	v_add_co_u32_e32 v6, vcc, s29, v10
	s_nop 1
	v_addc_co_u32_e32 v7, vcc, 0, v11, vcc
	v_mfma_f32_16x16x32_bf16 v[86:89], v[82:85], v[18:21], v[62:65]
	global_load_dwordx4 v[46:49], v[10:11], off
	global_load_dwordx4 v[30:33], v[10:11], off offset:1024
	global_load_dwordx4 v[18:21], v[10:11], off offset:2048
	global_load_dwordx4 v[2:5], v[10:11], off offset:3072
	global_load_dwordx4 v[38:41], v[12:13], off offset:1024
	global_load_dwordx4 v[22:25], v[12:13], off offset:2048
	global_load_dwordx4 v[54:57], v[6:7], off offset:-4096
	global_load_dwordx4 v[58:61], v[6:7], off
	global_load_dwordx4 v[42:45], v[6:7], off offset:1024
	global_load_dwordx4 v[26:29], v[6:7], off offset:2048
	s_nop 0
	global_load_dwordx4 v[6:9], v[6:7], off offset:3072
	v_add_co_u32_e32 v10, vcc, s47, v10
	v_mfma_f32_16x16x32_bf16 v[78:81], v[78:81], v[246:249], v[176:179]
	s_nop 0
	v_addc_co_u32_e32 v11, vcc, 0, v11, vcc
	global_load_dwordx4 v[14:17], v[12:13], off offset:3072
	global_load_dwordx4 v[62:65], v[10:11], off
	global_load_dwordx4 v[50:53], v[10:11], off offset:1024
	global_load_dwordx4 v[34:37], v[10:11], off offset:2048
	s_nop 0
	global_load_dwordx4 v[10:13], v[10:11], off offset:3072
	v_exp_f32_e32 v176, v146
	v_exp_f32_e32 v177, v147
	v_pk_add_f32 v[146:147], v[150:151], 1.0 op_sel_hi:[1,0]
	v_mfma_f32_16x16x32_bf16 v[82:85], v[82:85], v[246:249], v[180:183]
	v_add_f32_e64 v176, v176, 1.0
	v_add_f32_e64 v177, v177, 1.0
	v_pk_mul_f32 v[150:151], v[146:147], v[176:177]
	s_nop 0
	v_rcp_f32_e32 v178, v150
	v_rcp_f32_e32 v179, v151
	v_add_u32_e32 v150, v245, v197
	v_add_u32_e32 v154, v150, v198
	ds_read_b64 v[150:151], v154
	v_pk_mul_f32 v[176:177], v[176:177], v[178:179]
	s_waitcnt vmcnt(17)
	v_pk_mul_f32 v[176:177], v[110:111], v[176:177]
	s_nop 0
	v_pk_add_f32 v[182:183], v[176:177], v[176:177]
	s_nop 0
	v_pk_fma_f32 v[180:181], v[182:183], s[46:47], v[164:165] op_sel_hi:[1,0,0]
	v_min_f32_e32 v170, v182, v183
	v_pk_fma_f32 v[180:181], v[182:183], v[180:181], 0.5 op_sel_hi:[1,1,0]
	v_cmp_ge_f32_e32 vcc, s66, v170
	v_pk_fma_f32 v[180:181], v[182:183], v[180:181], 1.0 op_sel_hi:[1,1,0]
	s_nop 0
	v_pk_mul_f32 v[180:181], v[180:181], v[182:183] neg_lo:[0,1] neg_hi:[0,1]
	s_and_saveexec_b64 s[52:53], vcc
	s_cbranch_execnz .LBB0_1308

.LBB0_1752:
	s_waitcnt lgkmcnt(2)
	v_and_b32_e32 v209, 0xffff0000, v201
	v_and_b32_e32 v208, 0xffff0000, v193
	s_waitcnt lgkmcnt(1)
	v_lshlrev_b32_e32 v211, 16, v199
	v_lshlrev_b32_e32 v210, 16, v198
	v_and_b32_e32 v199, 0xffff0000, v199
	v_and_b32_e32 v198, 0xffff0000, v198
	v_lshlrev_b32_e32 v207, 16, v201
	v_lshlrev_b32_e32 v206, 16, v193
	v_lshlrev_b32_e32 v212, 16, v196
	s_waitcnt lgkmcnt(0)
	v_and_b32_e32 v213, 0xffff0000, v196
	v_lshlrev_b32_e32 v196, 16, v197
	v_lshlrev_b32_e32 v214, 16, v194
	v_pk_mul_f32 v[192:193], v[208:209], v[208:209]
	v_pk_mul_f32 v[216:217], v[198:199], v[198:199]
	v_and_b32_e32 v197, 0xffff0000, v197
	v_pk_fma_f32 v[192:193], v[206:207], v[206:207], v[192:193]
	v_pk_fma_f32 v[216:217], v[210:211], v[210:211], v[216:217]
	v_mul_f32_e32 v215, v212, v212
	v_mul_f32_e32 v219, v213, v213
	v_mul_f32_e32 v170, v196, v196
	v_mov_b32_e32 v218, v214
	v_and_b32_e32 v201, 0xffff0000, v194
	v_lshlrev_b32_e32 v194, 16, v195
	v_and_b32_e32 v195, 0xffff0000, v195
	v_pk_add_f32 v[192:193], v[192:193], v[192:193] op_sel_hi:[0,1]
	v_pk_add_f32 v[216:217], v[216:217], v[216:217] op_sel_hi:[0,1]
	v_pk_fma_f32 v[220:221], v[196:197], v[196:197], v[170:171] op_sel_hi:[1,1,0]
	v_pk_add_f32 v[218:219], v[214:215], v[218:219]
	v_mul_f32_e32 v220, v201, v201
	v_mul_f32_e32 v192, v194, v194
	v_mul_f32_e32 v216, v195, v195
	v_mul_f32_e32 v222, v214, v214
	v_mov_b32_e32 v223, v219
	v_pk_add_f32 v[218:219], v[222:223], v[220:221]
	v_pk_add_f32 v[192:193], v[192:193], v[216:217]
	v_mov_b32_e32 v224, 0
	v_pk_add_f32 v[192:193], v[218:219], v[192:193]
	v_mov_b32_e32 v215, v201
	v_add_f32_e32 v170, v192, v193
	s_nop 1
	v_add_f32_dpp v237, v170, v170 quad_perm:[1,0,3,2] row_mask:0xf bank_mask:0xf
	s_nop 1
	v_add_f32_dpp v237, v237, v237 quad_perm:[2,3,0,1] row_mask:0xf bank_mask:0xf
	s_nop 1
	v_add_f32_dpp v237, v237, v237 row_half_mirror row_mask:0xf bank_mask:0xf
	s_nop 1
	v_add_f32_dpp v237, v237, v237 row_mirror row_mask:0xf bank_mask:0xf
	s_nop 0
	v_mov_b32_e32 v236, v237
	s_nop 1
	v_permlane16_swap_b32_e32 v237, v236
	s_nop 0
	v_add_f32_e32 v237, v237, v236
	v_mov_b32_e32 v236, v237
	s_nop 1
	v_permlane32_swap_b32_e32 v237, v236
	s_nop 0
	v_add_f32_e32 v237, v237, v236
	v_mov_b32_e32 v193, v208
	v_mov_b32_e32 v208, v207
	s_waitcnt lgkmcnt(0)
	s_waitcnt lgkmcnt(0)
	s_waitcnt lgkmcnt(0)
	s_waitcnt lgkmcnt(0)
	s_waitcnt lgkmcnt(0)
	s_waitcnt lgkmcnt(0)
	v_mov_b32_e32 v170, v237
	v_fmamk_f32 v170, v170, 0x3a800000, v167
	v_mul_f32_e32 v192, 0x4b800000, v170
	v_cmp_gt_f32_e32 vcc, s23, v170
	s_nop 1
	v_cndmask_b32_e32 v170, v170, v192, vcc
	v_rsq_f32_e32 v170, v170
	s_nop 0
	v_mul_f32_e32 v192, 0x45800000, v170
	v_cndmask_b32_e32 v170, v170, v192, vcc
	v_mov_b32_e32 v192, v206
	v_pk_mul_f32 v[192:193], v[170:171], v[192:193] op_sel_hi:[0,1]
	s_waitcnt vmcnt(3)
	v_pk_fma_f32 v[216:217], v[146:147], v[192:193], v[138:139]
	v_pk_mul_f32 v[192:193], v[170:171], v[208:209] op_sel_hi:[0,1]
	v_cvt_pk_fp8_f32 v224, v216, v217
	v_pk_fma_f32 v[208:209], v[14:15], v[216:217], 0 op_sel_hi:[1,0,0]
	v_pk_fma_f32 v[218:219], v[16:17], v[216:217], 0 op_sel_hi:[1,0,0]
	v_pk_fma_f32 v[220:221], v[10:11], v[216:217], 0 op_sel_hi:[1,0,0]
	v_pk_fma_f32 v[222:223], v[12:13], v[216:217], 0 op_sel_hi:[1,0,0]
	v_pk_fma_f32 v[206:207], v[148:149], v[192:193], v[140:141]
	v_pk_fma_f32 v[218:219], v[8:9], v[216:217], v[218:219] op_sel:[0,1,0]
	v_pk_fma_f32 v[208:209], v[6:7], v[216:217], v[208:209] op_sel:[0,1,0]
	v_pk_fma_f32 v[222:223], v[4:5], v[216:217], v[222:223] op_sel:[0,1,0]
	v_pk_fma_f32 v[216:217], v[2:3], v[216:217], v[220:221] op_sel:[0,1,0]
	v_pk_fma_f32 v[208:209], v[30:31], v[206:207], v[208:209] op_sel_hi:[1,0,1]
	v_pk_fma_f32 v[218:219], v[32:33], v[206:207], v[218:219] op_sel_hi:[1,0,1]
	v_pk_fma_f32 v[216:217], v[26:27], v[206:207], v[216:217] op_sel_hi:[1,0,1]
	v_pk_fma_f32 v[220:221], v[28:29], v[206:207], v[222:223] op_sel_hi:[1,0,1]
	v_cvt_pk_fp8_f32 v224, v206, v207 op_sel:[0,0,1]
	v_pk_fma_f32 v[218:219], v[24:25], v[206:207], v[218:219] op_sel:[0,1,0]
	v_pk_fma_f32 v[208:209], v[22:23], v[206:207], v[208:209] op_sel:[0,1,0]
	v_pk_fma_f32 v[220:221], v[20:21], v[206:207], v[220:221] op_sel:[0,1,0]
	v_pk_fma_f32 v[206:207], v[18:19], v[206:207], v[216:217] op_sel:[0,1,0]
	v_mov_b32_e32 v216, v210
	v_mov_b32_e32 v217, v198
	v_pk_mul_f32 v[216:217], v[170:171], v[216:217] op_sel_hi:[0,1]
	s_waitcnt vmcnt(2)
	v_pk_fma_f32 v[216:217], v[150:151], v[216:217], v[134:135]
	v_mov_b32_e32 v222, 0
	v_mov_b32_e32 v198, v211
	v_cvt_pk_fp8_f32 v222, v216, v217
	v_pk_mul_f32 v[198:199], v[170:171], v[198:199] op_sel_hi:[0,1]
	v_pk_fma_f32 v[208:209], v[46:47], v[216:217], v[208:209] op_sel_hi:[1,0,1]
	v_pk_fma_f32 v[198:199], v[152:153], v[198:199], v[136:137]
	v_pk_fma_f32 v[210:211], v[48:49], v[216:217], v[218:219] op_sel_hi:[1,0,1]
	v_pk_fma_f32 v[206:207], v[42:43], v[216:217], v[206:207] op_sel_hi:[1,0,1]
	v_pk_fma_f32 v[218:219], v[44:45], v[216:217], v[220:221] op_sel_hi:[1,0,1]
	v_pk_fma_f32 v[208:209], v[38:39], v[216:217], v[208:209] op_sel:[0,1,0]
	v_pk_fma_f32 v[210:211], v[40:41], v[216:217], v[210:211] op_sel:[0,1,0]
	v_pk_fma_f32 v[218:219], v[36:37], v[216:217], v[218:219] op_sel:[0,1,0]
	v_pk_fma_f32 v[206:207], v[34:35], v[216:217], v[206:207] op_sel:[0,1,0]
	v_pk_fma_f32 v[208:209], v[50:51], v[198:199], v[208:209] op_sel_hi:[1,0,1]
	v_pk_mul_f32 v[212:213], v[212:213], v[170:171] op_sel_hi:[1,0]
	v_pk_fma_f32 v[210:211], v[52:53], v[198:199], v[210:211] op_sel_hi:[1,0,1]
	v_pk_fma_f32 v[206:207], v[62:63], v[198:199], v[206:207] op_sel_hi:[1,0,1]
	v_pk_fma_f32 v[216:217], v[64:65], v[198:199], v[218:219] op_sel_hi:[1,0,1]
	v_pk_fma_f32 v[208:209], v[58:59], v[198:199], v[208:209] op_sel:[0,1,0]
	s_waitcnt vmcnt(1)
	v_pk_fma_f32 v[212:213], v[154:155], v[212:213], v[130:131]
	v_cvt_pk_fp8_f32 v222, v198, v199 op_sel:[0,0,1]
	v_pk_fma_f32 v[210:211], v[60:61], v[198:199], v[210:211] op_sel:[0,1,0]
	v_pk_fma_f32 v[216:217], v[56:57], v[198:199], v[216:217] op_sel:[0,1,0]
	v_pk_fma_f32 v[198:199], v[54:55], v[198:199], v[206:207] op_sel:[0,1,0]
	v_pk_mul_f32 v[196:197], v[196:197], v[170:171] op_sel_hi:[1,0]
	v_pk_fma_f32 v[206:207], v[78:79], v[212:213], v[208:209] op_sel_hi:[1,0,1]
	v_mov_b32_e32 v218, 0
	v_pk_fma_f32 v[196:197], v[156:157], v[196:197], v[132:133]
	v_pk_fma_f32 v[208:209], v[80:81], v[212:213], v[210:211] op_sel_hi:[1,0,1]
	v_pk_fma_f32 v[198:199], v[74:75], v[212:213], v[198:199] op_sel_hi:[1,0,1]
	v_pk_fma_f32 v[210:211], v[76:77], v[212:213], v[216:217] op_sel_hi:[1,0,1]
	v_pk_fma_f32 v[206:207], v[70:71], v[212:213], v[206:207] op_sel:[0,1,0]
	v_cvt_pk_fp8_f32 v218, v212, v213
	v_pk_fma_f32 v[208:209], v[72:73], v[212:213], v[208:209] op_sel:[0,1,0]
	v_pk_fma_f32 v[210:211], v[68:69], v[212:213], v[210:211] op_sel:[0,1,0]
	v_pk_fma_f32 v[198:199], v[66:67], v[212:213], v[198:199] op_sel:[0,1,0]
	v_pk_fma_f32 v[206:207], v[82:83], v[196:197], v[206:207] op_sel_hi:[1,0,1]
	v_pk_mul_f32 v[212:213], v[214:215], v[170:171] op_sel_hi:[1,0]
	v_pk_fma_f32 v[206:207], v[90:91], v[196:197], v[206:207] op_sel:[0,1,0]
	s_waitcnt vmcnt(0)
	v_pk_fma_f32 v[212:213], v[158:159], v[212:213], v[142:143]
	v_pk_mul_f32 v[194:195], v[194:195], v[170:171] op_sel_hi:[1,0]
	v_pk_fma_f32 v[206:207], v[110:111], v[212:213], v[206:207] op_sel_hi:[1,0,1]
	v_pk_fma_f32 v[194:195], v[160:161], v[194:195], v[144:145]
	v_pk_fma_f32 v[206:207], v[102:103], v[212:213], v[206:207] op_sel:[0,1,0]
	v_pk_fma_f32 v[208:209], v[84:85], v[196:197], v[208:209] op_sel_hi:[1,0,1]
	v_pk_fma_f32 v[206:207], v[114:115], v[194:195], v[206:207] op_sel_hi:[1,0,1]
	v_pk_fma_f32 v[198:199], v[94:95], v[196:197], v[198:199] op_sel_hi:[1,0,1]
	v_pk_fma_f32 v[206:207], v[122:123], v[194:195], v[206:207] op_sel:[0,1,0]
	s_nop 1
	v_add_f32_dpp v249, v206, v206 quad_perm:[1,0,3,2] row_mask:0xf bank_mask:0xf
	s_nop 1
	v_add_f32_dpp v249, v249, v249 quad_perm:[2,3,0,1] row_mask:0xf bank_mask:0xf
	s_nop 1
	v_add_f32_dpp v249, v249, v249 row_half_mirror row_mask:0xf bank_mask:0xf
	s_nop 1
	v_add_f32_dpp v249, v249, v249 row_mirror row_mask:0xf bank_mask:0xf
	s_nop 0
	v_mov_b32_e32 v236, v249
	s_nop 1
	v_permlane16_swap_b32_e32 v249, v236
	s_nop 0
	v_add_f32_e32 v249, v249, v236
	v_mov_b32_e32 v236, v249
	s_nop 1
	v_permlane32_swap_b32_e32 v249, v236
	s_nop 0
	v_add_f32_e32 v249, v249, v236
	s_nop 1
	v_add_f32_dpp v248, v207, v207 quad_perm:[1,0,3,2] row_mask:0xf bank_mask:0xf
	s_nop 1
	v_add_f32_dpp v248, v248, v248 quad_perm:[2,3,0,1] row_mask:0xf bank_mask:0xf
	s_nop 1
	v_add_f32_dpp v248, v248, v248 row_half_mirror row_mask:0xf bank_mask:0xf
	s_nop 1
	v_add_f32_dpp v248, v248, v248 row_mirror row_mask:0xf bank_mask:0xf
	s_nop 0
	v_mov_b32_e32 v236, v248
	s_nop 1
	v_permlane16_swap_b32_e32 v248, v236
	s_nop 0
	v_add_f32_e32 v248, v248, v236
	v_mov_b32_e32 v236, v248
	s_nop 1
	v_permlane32_swap_b32_e32 v248, v236
	s_nop 0
	v_add_f32_e32 v248, v248, v236
	v_pk_fma_f32 v[210:211], v[96:97], v[196:197], v[210:211] op_sel_hi:[1,0,1]
	v_pk_fma_f32 v[208:209], v[92:93], v[196:197], v[208:209] op_sel:[0,1,0]
	v_cvt_pk_fp8_f32 v218, v196, v197 op_sel:[0,0,1]
	v_pk_fma_f32 v[210:211], v[88:89], v[196:197], v[210:211] op_sel:[0,1,0]
	s_waitcnt lgkmcnt(0)
	v_pk_fma_f32 v[196:197], v[86:87], v[196:197], v[198:199] op_sel:[0,1,0]
	v_pk_fma_f32 v[198:199], v[112:113], v[212:213], v[208:209] op_sel_hi:[1,0,1]
	v_pk_fma_f32 v[198:199], v[104:105], v[212:213], v[198:199] op_sel:[0,1,0]
	v_mov_b32_e32 v170, 0
	v_pk_fma_f32 v[198:199], v[116:117], v[194:195], v[198:199] op_sel_hi:[1,0,1]
	v_cvt_pk_fp8_f32 v170, v212, v213
	s_waitcnt lgkmcnt(0)
	v_pk_fma_f32 v[198:199], v[124:125], v[194:195], v[198:199] op_sel:[0,1,0]
	s_nop 1
	v_add_f32_dpp v237, v198, v198 quad_perm:[1,0,3,2] row_mask:0xf bank_mask:0xf
	s_nop 1
	v_add_f32_dpp v237, v237, v237 quad_perm:[2,3,0,1] row_mask:0xf bank_mask:0xf
	s_nop 1
	v_add_f32_dpp v237, v237, v237 row_half_mirror row_mask:0xf bank_mask:0xf
	s_nop 1
	v_add_f32_dpp v237, v237, v237 row_mirror row_mask:0xf bank_mask:0xf
	s_nop 0
	v_mov_b32_e32 v236, v237
	s_nop 1
	v_permlane16_swap_b32_e32 v237, v236
	s_nop 0
	v_add_f32_e32 v237, v237, v236
	v_mov_b32_e32 v236, v237
	s_nop 1
	v_permlane32_swap_b32_e32 v237, v236
	s_nop 0
	v_add_f32_e32 v237, v237, v236
	v_pk_fma_f32 v[196:197], v[106:107], v[212:213], v[196:197] op_sel_hi:[1,0,1]
	v_pk_fma_f32 v[210:211], v[108:109], v[212:213], v[210:211] op_sel_hi:[1,0,1]
	s_waitcnt lgkmcnt(1)
	s_waitcnt lgkmcnt(2)
	v_pk_fma_f32 v[210:211], v[100:101], v[212:213], v[210:211] op_sel:[0,1,0]
	v_pk_fma_f32 v[196:197], v[98:99], v[212:213], v[196:197] op_sel:[0,1,0]
	v_pk_fma_f32 v[210:211], v[128:129], v[194:195], v[210:211] op_sel_hi:[1,0,1]
	v_pk_fma_f32 v[196:197], v[126:127], v[194:195], v[196:197] op_sel_hi:[1,0,1]
	v_cvt_pk_fp8_f32 v170, v194, v195 op_sel:[0,0,1]
	v_pk_fma_f32 v[210:211], v[120:121], v[194:195], v[210:211] op_sel:[0,1,0]
	v_pk_fma_f32 v[212:213], v[118:119], v[194:195], v[196:197] op_sel:[0,1,0]
	s_waitcnt lgkmcnt(1)
	s_nop 1
	v_add_f32_dpp v238, v199, v199 quad_perm:[1,0,3,2] row_mask:0xf bank_mask:0xf
	s_nop 1
	v_add_f32_dpp v238, v238, v238 quad_perm:[2,3,0,1] row_mask:0xf bank_mask:0xf
	s_nop 1
	v_add_f32_dpp v238, v238, v238 row_half_mirror row_mask:0xf bank_mask:0xf
	s_nop 1
	v_add_f32_dpp v238, v238, v238 row_mirror row_mask:0xf bank_mask:0xf
	s_nop 0
	v_mov_b32_e32 v236, v238
	s_nop 1
	v_permlane16_swap_b32_e32 v238, v236
	s_nop 0
	v_add_f32_e32 v238, v238, v236
	v_mov_b32_e32 v236, v238
	s_nop 1
	v_permlane32_swap_b32_e32 v238, v236
	s_nop 0
	v_add_f32_e32 v238, v238, v236
	s_waitcnt lgkmcnt(3)
	s_nop 1
	v_add_f32_dpp v239, v212, v212 quad_perm:[1,0,3,2] row_mask:0xf bank_mask:0xf
	s_nop 1
	v_add_f32_dpp v239, v239, v239 quad_perm:[2,3,0,1] row_mask:0xf bank_mask:0xf
	s_nop 1
	v_add_f32_dpp v239, v239, v239 row_half_mirror row_mask:0xf bank_mask:0xf
	s_nop 1
	v_add_f32_dpp v239, v239, v239 row_mirror row_mask:0xf bank_mask:0xf
	s_nop 0
	v_mov_b32_e32 v236, v239
	s_nop 1
	v_permlane16_swap_b32_e32 v239, v236
	s_nop 0
	v_add_f32_e32 v239, v239, v236
	v_mov_b32_e32 v236, v239
	s_nop 1
	v_permlane32_swap_b32_e32 v239, v236
	s_nop 0
	v_add_f32_e32 v239, v239, v236
	s_waitcnt lgkmcnt(3)
	s_waitcnt lgkmcnt(2)
	s_waitcnt lgkmcnt(2)
	s_waitcnt lgkmcnt(1)
	s_waitcnt lgkmcnt(2)
	s_nop 1
	v_add_f32_dpp v240, v213, v213 quad_perm:[1,0,3,2] row_mask:0xf bank_mask:0xf
	s_nop 1
	v_add_f32_dpp v240, v240, v240 quad_perm:[2,3,0,1] row_mask:0xf bank_mask:0xf
	s_nop 1
	v_add_f32_dpp v240, v240, v240 row_half_mirror row_mask:0xf bank_mask:0xf
	s_nop 1
	v_add_f32_dpp v240, v240, v240 row_mirror row_mask:0xf bank_mask:0xf
	s_nop 0
	v_mov_b32_e32 v236, v240
	s_nop 1
	v_permlane16_swap_b32_e32 v240, v236
	s_nop 0
	v_add_f32_e32 v240, v240, v236
	v_mov_b32_e32 v236, v240
	s_nop 1
	v_permlane32_swap_b32_e32 v240, v236
	s_nop 0
	v_add_f32_e32 v240, v240, v236
	s_waitcnt lgkmcnt(3)
	s_waitcnt lgkmcnt(3)
	s_waitcnt lgkmcnt(2)
	s_waitcnt lgkmcnt(2)
	s_nop 1
	v_add_f32_dpp v241, v211, v211 quad_perm:[1,0,3,2] row_mask:0xf bank_mask:0xf
	s_nop 1
	v_add_f32_dpp v241, v241, v241 quad_perm:[2,3,0,1] row_mask:0xf bank_mask:0xf
	s_nop 1
	v_add_f32_dpp v241, v241, v241 row_half_mirror row_mask:0xf bank_mask:0xf
	s_nop 1
	v_add_f32_dpp v241, v241, v241 row_mirror row_mask:0xf bank_mask:0xf
	s_nop 0
	v_mov_b32_e32 v236, v241
	s_nop 1
	v_permlane16_swap_b32_e32 v241, v236
	s_nop 0
	v_add_f32_e32 v241, v241, v236
	v_mov_b32_e32 v236, v241
	s_nop 1
	v_permlane32_swap_b32_e32 v241, v236
	s_nop 0
	v_add_f32_e32 v241, v241, v236
	s_waitcnt lgkmcnt(3)
	s_waitcnt lgkmcnt(2)
	s_waitcnt lgkmcnt(2)
	s_waitcnt lgkmcnt(2)
	s_waitcnt lgkmcnt(1)
	s_waitcnt lgkmcnt(1)
	s_nop 1
	v_add_f32_dpp v242, v210, v210 quad_perm:[1,0,3,2] row_mask:0xf bank_mask:0xf
	s_nop 1
	v_add_f32_dpp v242, v242, v242 quad_perm:[2,3,0,1] row_mask:0xf bank_mask:0xf
	s_nop 1
	v_add_f32_dpp v242, v242, v242 row_half_mirror row_mask:0xf bank_mask:0xf
	s_nop 1
	v_add_f32_dpp v242, v242, v242 row_mirror row_mask:0xf bank_mask:0xf
	s_nop 0
	v_mov_b32_e32 v236, v242
	s_nop 1
	v_permlane16_swap_b32_e32 v242, v236
	s_nop 0
	v_add_f32_e32 v242, v242, v236
	v_mov_b32_e32 v236, v242
	s_nop 1
	v_permlane32_swap_b32_e32 v242, v236
	s_nop 0
	v_add_f32_e32 v242, v242, v236
	s_waitcnt lgkmcnt(3)
	s_waitcnt lgkmcnt(3)
	s_waitcnt lgkmcnt(3)
	s_waitcnt lgkmcnt(2)
	s_waitcnt lgkmcnt(2)
	s_waitcnt lgkmcnt(2)
	s_waitcnt lgkmcnt(2)
	s_waitcnt lgkmcnt(2)
	s_waitcnt lgkmcnt(2)
	s_waitcnt lgkmcnt(3)
	s_waitcnt lgkmcnt(3)
	s_waitcnt lgkmcnt(2)
	v_lshl_add_u64 v[192:193], s[72:73], 0, v[180:181]
	v_add_co_u32_e32 v192, vcc, s35, v192
	s_nop 1
	v_addc_co_u32_e32 v193, vcc, 0, v193, vcc
	global_store_dword v[192:193], v224, off
	global_store_dword v[192:193], v222, off offset:256
	global_store_dword v[192:193], v218, off offset:512
	global_store_dword v[192:193], v170, off offset:768
	s_and_saveexec_b64 s[44:45], s[4:5]
	s_cbranch_execz .LBB0_1747
	v_mov_b32_e32 v192, v249
	v_mov_b32_e32 v193, v248
	v_mov_b32_e32 v198, v237
	v_cmp_gt_f32_e32 vcc, v193, v192
	s_waitcnt lgkmcnt(4)
	v_mov_b32_e32 v201, v238
	s_waitcnt lgkmcnt(3)
	v_mov_b32_e32 v206, v239
	v_cndmask_b32_e32 v194, v192, v193, vcc
	v_cmp_gt_f32_e64 s[6:7], v198, v194
	s_waitcnt lgkmcnt(2)
	v_mov_b32_e32 v208, v240
	v_cndmask_b32_e64 v195, 0, 1, vcc
	v_cndmask_b32_e64 v194, v194, v198, s[6:7]
	v_cmp_gt_f32_e64 s[8:9], v201, v194
	v_cndmask_b32_e64 v195, v195, 2, s[6:7]
	s_waitcnt lgkmcnt(1)
	v_mov_b32_e32 v210, v242
	v_cndmask_b32_e64 v194, v194, v201, s[8:9]
	v_cmp_gt_f32_e64 s[10:11], v206, v194
	v_cndmask_b32_e64 v195, v195, 3, s[8:9]
	s_waitcnt lgkmcnt(0)
	v_mov_b32_e32 v170, v241
	v_cndmask_b32_e64 v194, v194, v206, s[10:11]
	v_cmp_gt_f32_e64 s[12:13], v208, v194
	v_cndmask_b32_e64 v195, v195, 4, s[10:11]
	s_ashr_i32 s39, s38, 31
	v_cndmask_b32_e64 v194, v194, v208, s[12:13]
	v_cmp_gt_f32_e64 s[14:15], v210, v194
	v_cndmask_b32_e64 v195, v195, 5, s[12:13]
	s_lshl_b64 s[6:7], s[38:39], 2
	v_cndmask_b32_e64 v194, v194, v210, s[14:15]
	v_cmp_ngt_f32_e64 s[16:17], v170, v194
	v_cndmask_b32_e64 v195, v195, 6, s[14:15]
	s_and_b64 s[20:21], s[14:15], s[16:17]
	v_cndmask_b32_e64 v195, 7, v195, s[16:17]
	v_cmp_nlt_f32_e32 vcc, s46, v192
	s_add_u32 s48, s30, s6
	v_cmp_eq_u32_e64 s[18:19], 0, v195
	s_addc_u32 s49, s31, s7
	s_or_b64 vcc, s[18:19], vcc
	v_cndmask_b32_e32 v192, v192, v177, vcc
	v_cmp_ne_u32_e64 s[14:15], 1, v195
	v_cmp_gt_f32_e64 s[18:19], v193, v192
	s_and_b64 s[14:15], s[14:15], s[18:19]
	v_cndmask_b32_e64 v192, v192, v193, s[14:15]
	v_cmp_ne_u32_e64 s[12:13], 2, v195
	v_cmp_gt_f32_e64 s[18:19], v198, v192
	s_and_b64 s[12:13], s[12:13], s[18:19]
	v_cndmask_b32_e64 v192, v192, v198, s[12:13]
	v_cmp_ne_u32_e64 s[10:11], 3, v195
	v_cmp_gt_f32_e64 s[18:19], v201, v192
	s_and_b64 s[10:11], s[10:11], s[18:19]
	v_cndmask_b32_e64 v192, v192, v201, s[10:11]
	v_cmp_ne_u32_e64 s[8:9], 4, v195
	v_cmp_gt_f32_e64 s[18:19], v206, v192
	s_and_b64 s[8:9], s[8:9], s[18:19]
	v_cndmask_b32_e64 v192, v192, v206, s[8:9]
	v_cmp_ne_u32_e64 s[6:7], 5, v195
	v_cmp_gt_f32_e64 s[18:19], v208, v192
	s_and_b64 s[6:7], s[6:7], s[18:19]
	v_cndmask_b32_e64 v192, v192, v208, s[6:7]
	v_cmp_ngt_f32_e64 s[18:19], v210, v192
	s_or_b64 s[18:19], s[20:21], s[18:19]
	v_cndmask_b32_e64 v194, v170, v194, s[16:17]
	v_cndmask_b32_e64 v192, v210, v192, s[18:19]
	v_cmp_gt_f32_e64 s[20:21], v170, v192
	s_and_b64 s[16:17], s[16:17], s[20:21]
	v_cndmask_b32_e64 v170, v192, v170, s[16:17]
	v_sub_f32_e32 v170, v170, v194
	v_mul_f32_e32 v170, 0x3fb8aa3b, v170
	v_exp_f32_e32 v170, v170
	v_cndmask_b32_e64 v192, 0, -1, vcc
	v_cndmask_b32_e64 v192, v192, 1, s[14:15]
	v_cndmask_b32_e64 v192, v192, 2, s[12:13]
	v_cndmask_b32_e64 v192, v192, 3, s[10:11]
	v_add_f32_e32 v170, 1.0, v170
	v_cndmask_b32_e64 v192, v192, 4, s[8:9]
	v_div_scale_f32 v193, s[8:9], v170, v170, 1.0
	v_rcp_f32_e32 v194, v193
	v_cndmask_b32_e64 v192, v192, 5, s[6:7]
	v_cndmask_b32_e64 v192, 6, v192, s[18:19]
	v_cndmask_b32_e64 v196, v192, 7, s[16:17]
	v_fma_f32 v192, -v193, v194, 1.0
	v_fmac_f32_e32 v194, v192, v194
	v_div_scale_f32 v192, vcc, 1.0, v170, 1.0
	v_mul_f32_e32 v197, v192, v194
	v_fma_f32 v198, -v193, v197, v192
	v_fmac_f32_e32 v197, v198, v194
	v_fma_f32 v192, -v193, v197, v192
	v_div_fmas_f32 v192, v192, v194, v197
	v_div_fixup_f32 v192, v192, v170, 1.0
	v_sub_f32_e32 v193, 1.0, v192
	global_store_dwordx2 v163, v[192:193], s[48:49]
	v_lshl_add_u32 v170, v195, 2, 0
	ds_add_rtn_u32 v170, v170, v173
	v_lshl_add_u32 v192, v196, 2, 0
	ds_add_rtn_u32 v192, v192, v173
	s_min_i32 s39, s33, 63
	s_lshl_b32 s6, s39, 3
	s_add_i32 s6, s34, s6
	v_lshlrev_b32_e32 v193, 16, v196
	v_lshlrev_b32_e32 v194, 16, v195
	s_waitcnt lgkmcnt(0)
	v_or_b32_e32 v193, v192, v193
	v_or_b32_e32 v192, v170, v194
	v_mov_b32_e32 v170, s6
	ds_write_b64 v170, v[192:193] offset:64
	s_branch .LBB0_1747

.LBB0_2168:
	v_cvt_pk_f32_fp8_e32 v[88:89], v82
	v_cvt_pk_f32_fp8_sdwa v[90:91], v82 src0_sel:WORD_1
	v_cvt_pk_f32_fp8_e32 v[64:65], v73
	v_cvt_pk_f32_fp8_sdwa v[86:87], v73 src0_sel:WORD_1
	v_pk_mul_f32 v[88:89], v[44:45], v[88:89] op_sel_hi:[0,1]
	v_pk_mul_f32 v[90:91], v[44:45], v[90:91] op_sel_hi:[0,1]
	v_lshlrev_b32_e32 v92, 16, v52
	v_and_b32_e32 v93, 0xffff0000, v52
	v_lshlrev_b32_e32 v94, 16, v53
	v_and_b32_e32 v95, 0xffff0000, v53
	v_pk_fma_f32 v[86:87], v[42:43], v[86:87], v[90:91] op_sel_hi:[0,1,1]
	v_pk_fma_f32 v[64:65], v[42:43], v[64:65], v[88:89] op_sel_hi:[0,1,1]
	s_waitcnt vmcnt(3)
	v_pk_fma_f32 v[64:65], v[18:19], v[64:65], v[92:93]
	v_pk_fma_f32 v[86:87], v[20:21], v[86:87], v[94:95]
	v_pk_mul_f32 v[90:91], v[64:65], v[64:65]
	v_pk_mul_f32 v[88:89], v[86:87], v[86:87]
	v_cvt_pk_f32_fp8_e32 v[94:95], v83
	v_pk_mov_b32 v[92:93], v[90:91], v[88:89] op_sel:[1,0]
	v_mov_b32_e32 v91, v89
	v_cvt_pk_f32_fp8_sdwa v[96:97], v83 src0_sel:WORD_1
	v_pk_add_f32 v[88:89], v[92:93], v[90:91]
	v_cvt_pk_f32_fp8_e32 v[90:91], v75
	v_cvt_pk_f32_fp8_sdwa v[92:93], v75 src0_sel:WORD_1
	v_pk_mul_f32 v[94:95], v[44:45], v[94:95] op_sel_hi:[0,1]
	v_pk_mul_f32 v[96:97], v[44:45], v[96:97] op_sel_hi:[0,1]
	v_lshlrev_b32_e32 v98, 16, v56
	v_and_b32_e32 v99, 0xffff0000, v56
	v_lshlrev_b32_e32 v100, 16, v57
	v_and_b32_e32 v101, 0xffff0000, v57
	v_pk_fma_f32 v[92:93], v[42:43], v[92:93], v[96:97] op_sel_hi:[0,1,1]
	v_pk_fma_f32 v[90:91], v[42:43], v[90:91], v[94:95] op_sel_hi:[0,1,1]
	s_waitcnt vmcnt(2)
	v_pk_fma_f32 v[90:91], v[22:23], v[90:91], v[98:99]
	v_pk_fma_f32 v[92:93], v[24:25], v[92:93], v[100:101]
	v_pk_mul_f32 v[96:97], v[90:91], v[90:91]
	v_pk_mul_f32 v[94:95], v[92:93], v[92:93]
	v_cvt_pk_f32_fp8_e32 v[100:101], v84
	v_pk_mov_b32 v[98:99], v[96:97], v[94:95] op_sel:[1,0]
	v_mov_b32_e32 v97, v95
	v_pk_add_f32 v[94:95], v[98:99], v[96:97]
	v_cvt_pk_f32_fp8_e32 v[96:97], v76
	v_cvt_pk_f32_fp8_sdwa v[102:103], v84 src0_sel:WORD_1
	v_cvt_pk_f32_fp8_sdwa v[98:99], v76 src0_sel:WORD_1
	v_pk_mul_f32 v[100:101], v[44:45], v[100:101] op_sel_hi:[0,1]
	v_lshlrev_b32_e32 v104, 16, v58
	v_and_b32_e32 v105, 0xffff0000, v58
	v_pk_fma_f32 v[96:97], v[42:43], v[96:97], v[100:101] op_sel_hi:[0,1,1]
	s_waitcnt vmcnt(1)
	v_pk_fma_f32 v[96:97], v[26:27], v[96:97], v[104:105]
	v_cvt_pk_f32_fp8_e32 v[104:105], v85
	v_pk_mul_f32 v[102:103], v[44:45], v[102:103] op_sel_hi:[0,1]
	v_cvt_pk_f32_fp8_e32 v[100:101], v78
	v_lshlrev_b32_e32 v106, 16, v59
	v_and_b32_e32 v107, 0xffff0000, v59
	v_pk_fma_f32 v[98:99], v[42:43], v[98:99], v[102:103] op_sel_hi:[0,1,1]
	v_pk_fma_f32 v[98:99], v[28:29], v[98:99], v[106:107]
	v_cvt_pk_f32_fp8_sdwa v[106:107], v85 src0_sel:WORD_1
	v_cvt_pk_f32_fp8_sdwa v[102:103], v78 src0_sel:WORD_1
	v_pk_mul_f32 v[104:105], v[44:45], v[104:105] op_sel_hi:[0,1]
	v_lshlrev_b32_e32 v108, 16, v60
	v_and_b32_e32 v109, 0xffff0000, v60
	v_pk_fma_f32 v[100:101], v[42:43], v[100:101], v[104:105] op_sel_hi:[0,1,1]
	s_waitcnt vmcnt(0)
	v_pk_fma_f32 v[100:101], v[30:31], v[100:101], v[108:109]
	v_pk_mul_f32 v[106:107], v[44:45], v[106:107] op_sel_hi:[0,1]
	v_mul_f32_e32 v63, v100, v100
	v_mul_f32_e32 v104, v101, v101
	v_pk_add_f32 v[88:89], v[88:89], v[88:89] op_sel:[0,1] op_sel_hi:[1,0]
	v_pk_add_f32 v[94:95], v[94:95], v[94:95] op_sel:[0,1] op_sel_hi:[1,0]
	v_lshlrev_b32_e32 v110, 16, v61
	v_and_b32_e32 v111, 0xffff0000, v61
	v_pk_fma_f32 v[102:103], v[42:43], v[102:103], v[106:107] op_sel_hi:[0,1,1]
	v_mov_b32_e32 v89, v63
	v_mov_b32_e32 v95, v104
	v_pk_fma_f32 v[102:103], v[32:33], v[102:103], v[110:111]
	v_pk_add_f32 v[88:89], v[88:89], v[94:95]
	v_mul_f32_e32 v94, v97, v97
	v_mul_f32_e32 v105, v102, v102
	v_pk_fma_f32 v[94:95], v[96:97], v[96:97], v[94:95] op_sel_hi:[1,1,0]
	v_mul_f32_e32 v104, v99, v99
	v_mul_f32_e32 v106, v103, v103
	v_mov_b32_e32 v95, v105
	v_pk_fma_f32 v[104:105], v[98:99], v[98:99], v[104:105] op_sel_hi:[1,1,0]
	s_nop 0
	v_mov_b32_e32 v105, v106
	v_pk_add_f32 v[94:95], v[94:95], v[104:105]
	s_nop 0
	v_pk_add_f32 v[88:89], v[88:89], v[94:95]
	s_nop 0
	v_add_f32_e32 v63, v88, v89
	v_and_b32_e32 v88, 64, v62
	v_add_u32_e32 v88, 64, v88
	v_xor_b32_e32 v89, 1, v62
	v_cmp_lt_i32_e32 vcc, v89, v88
	s_nop 1
	v_cndmask_b32_e32 v89, v62, v89, vcc
	v_lshlrev_b32_e32 v89, 2, v89
	s_nop 1
	v_add_f32_dpp v237, v63, v63 quad_perm:[1,0,3,2] row_mask:0xf bank_mask:0xf
	s_nop 1
	v_add_f32_dpp v237, v237, v237 quad_perm:[2,3,0,1] row_mask:0xf bank_mask:0xf
	s_nop 1
	v_add_f32_dpp v237, v237, v237 row_half_mirror row_mask:0xf bank_mask:0xf
	s_nop 1
	v_add_f32_dpp v237, v237, v237 row_mirror row_mask:0xf bank_mask:0xf
	s_nop 0
	v_mov_b32_e32 v236, v237
	s_nop 1
	v_permlane16_swap_b32_e32 v237, v236
	s_nop 0
	v_add_f32_e32 v237, v237, v236
	v_mov_b32_e32 v236, v237
	s_nop 1
	v_permlane32_swap_b32_e32 v237, v236
	s_nop 0
	v_add_f32_e32 v237, v237, v236
	s_waitcnt lgkmcnt(0)
	v_xor_b32_e32 v89, 2, v62
	v_cmp_lt_i32_e32 vcc, v89, v88
	s_nop 1
	v_cndmask_b32_e32 v89, v62, v89, vcc
	v_lshlrev_b32_e32 v89, 2, v89
	s_waitcnt lgkmcnt(0)
	v_xor_b32_e32 v89, 4, v62
	v_cmp_lt_i32_e32 vcc, v89, v88
	s_nop 1
	v_cndmask_b32_e32 v89, v62, v89, vcc
	v_lshlrev_b32_e32 v89, 2, v89
	s_waitcnt lgkmcnt(0)
	v_xor_b32_e32 v89, 8, v62
	v_cmp_lt_i32_e32 vcc, v89, v88
	s_nop 1
	v_cndmask_b32_e32 v89, v62, v89, vcc
	v_lshlrev_b32_e32 v89, 2, v89
	s_waitcnt lgkmcnt(0)
	v_xor_b32_e32 v89, 16, v62
	v_cmp_lt_i32_e32 vcc, v89, v88
	s_nop 1
	v_cndmask_b32_e32 v89, v62, v89, vcc
	v_lshlrev_b32_e32 v89, 2, v89
	s_waitcnt lgkmcnt(0)
	v_xor_b32_e32 v89, 32, v62
	v_cmp_lt_i32_e32 vcc, v89, v88
	s_nop 1
	v_cndmask_b32_e32 v88, v62, v89, vcc
	v_lshlrev_b32_e32 v88, 2, v88
	s_waitcnt lgkmcnt(0)
	v_mov_b32_e32 v63, v237
	v_fmamk_f32 v63, v63, 0x3a800000, v68
	v_mul_f32_e32 v88, 0x4b800000, v63
	v_cmp_gt_f32_e32 vcc, s35, v63
	s_nop 1
	v_cndmask_b32_e32 v63, v63, v88, vcc
	v_rsq_f32_e32 v63, v63
	s_nop 0
	v_mul_f32_e32 v88, 0x45800000, v63
	v_cndmask_b32_e32 v94, v63, v88, vcc
	v_pk_mul_f32 v[64:65], v[64:65], v[94:95] op_sel_hi:[1,0]
	v_pk_mul_f32 v[86:87], v[86:87], v[94:95] op_sel_hi:[1,0]
	s_nop 0
	v_pk_mul_f32 v[88:89], v[4:5], v[86:87]
	v_pk_mul_f32 v[86:87], v[2:3], v[64:65]
	global_store_dwordx4 v[40:41], v[86:89], off offset:-4096
	v_pk_mul_f32 v[64:65], v[90:91], v[94:95] op_sel_hi:[1,0]
	s_nop 0
	v_pk_mul_f32 v[86:87], v[92:93], v[94:95] op_sel_hi:[1,0]
	s_nop 0
	v_pk_mul_f32 v[88:89], v[8:9], v[86:87]
	v_pk_mul_f32 v[86:87], v[6:7], v[64:65]
	global_store_dwordx4 v[40:41], v[86:89], off offset:-3072
	v_pk_mul_f32 v[64:65], v[96:97], v[94:95] op_sel_hi:[1,0]
	s_nop 0
	v_pk_mul_f32 v[86:87], v[98:99], v[94:95] op_sel_hi:[1,0]
	s_nop 0
	v_pk_mul_f32 v[88:89], v[12:13], v[86:87]
	v_pk_mul_f32 v[86:87], v[10:11], v[64:65]
	global_store_dwordx4 v[40:41], v[86:89], off offset:-2048
	v_pk_mul_f32 v[64:65], v[100:101], v[94:95] op_sel_hi:[1,0]
	s_nop 0
	v_pk_mul_f32 v[86:87], v[102:103], v[94:95] op_sel_hi:[1,0]
	s_nop 0
	v_pk_mul_f32 v[88:89], v[16:17], v[86:87]
	v_pk_mul_f32 v[86:87], v[14:15], v[64:65]
	global_store_dwordx4 v[40:41], v[86:89], off offset:-1024
	s_andn2_b64 vcc, exec, s[0:1]
	s_cbranch_vccnz .LBB0_2159
.LBB0_2169:
	s_waitcnt vmcnt(6)
	v_cvt_pk_f32_fp8_e32 v[88:89], v77
	v_cvt_pk_f32_fp8_sdwa v[90:91], v77 src0_sel:WORD_1
	v_cvt_pk_f32_fp8_e32 v[64:65], v70
	v_cvt_pk_f32_fp8_sdwa v[86:87], v70 src0_sel:WORD_1
	v_pk_mul_f32 v[88:89], v[44:45], v[88:89] op_sel:[1,0]
	v_pk_mul_f32 v[90:91], v[44:45], v[90:91] op_sel:[1,0]
	v_lshlrev_b32_e32 v92, 16, v46
	v_and_b32_e32 v93, 0xffff0000, v46
	v_lshlrev_b32_e32 v94, 16, v47
	v_and_b32_e32 v95, 0xffff0000, v47
	v_pk_fma_f32 v[86:87], v[42:43], v[86:87], v[90:91] op_sel:[1,0,0]
	v_pk_fma_f32 v[64:65], v[42:43], v[64:65], v[88:89] op_sel:[1,0,0]
	s_waitcnt vmcnt(3)
	v_pk_fma_f32 v[86:87], v[20:21], v[86:87], v[94:95]
	v_pk_fma_f32 v[64:65], v[18:19], v[64:65], v[92:93]
	v_pk_mul_f32 v[88:89], v[86:87], v[86:87]
	v_pk_mul_f32 v[90:91], v[64:65], v[64:65]
	v_cvt_pk_f32_fp8_e32 v[94:95], v79
	v_pk_mov_b32 v[92:93], v[90:91], v[88:89] op_sel:[1,0]
	v_mov_b32_e32 v91, v89
	v_cvt_pk_f32_fp8_sdwa v[96:97], v79 src0_sel:WORD_1
	v_pk_add_f32 v[88:89], v[92:93], v[90:91]
	v_cvt_pk_f32_fp8_e32 v[90:91], v71
	v_cvt_pk_f32_fp8_sdwa v[92:93], v71 src0_sel:WORD_1
	v_pk_mul_f32 v[94:95], v[44:45], v[94:95] op_sel:[1,0]
	v_pk_mul_f32 v[96:97], v[44:45], v[96:97] op_sel:[1,0]
	v_lshlrev_b32_e32 v98, 16, v48
	v_and_b32_e32 v99, 0xffff0000, v48
	v_lshlrev_b32_e32 v100, 16, v49
	v_and_b32_e32 v101, 0xffff0000, v49
	v_pk_fma_f32 v[92:93], v[42:43], v[92:93], v[96:97] op_sel:[1,0,0]
	v_pk_fma_f32 v[90:91], v[42:43], v[90:91], v[94:95] op_sel:[1,0,0]
	s_waitcnt vmcnt(2)
	v_pk_fma_f32 v[92:93], v[24:25], v[92:93], v[100:101]
	v_pk_fma_f32 v[90:91], v[22:23], v[90:91], v[98:99]
	v_pk_mul_f32 v[94:95], v[92:93], v[92:93]
	v_pk_mul_f32 v[96:97], v[90:91], v[90:91]
	v_cvt_pk_f32_fp8_e32 v[100:101], v80
	v_pk_mov_b32 v[98:99], v[96:97], v[94:95] op_sel:[1,0]
	v_mov_b32_e32 v97, v95
	v_pk_add_f32 v[94:95], v[98:99], v[96:97]
	v_cvt_pk_f32_fp8_e32 v[96:97], v72
	v_cvt_pk_f32_fp8_sdwa v[102:103], v80 src0_sel:WORD_1
	v_cvt_pk_f32_fp8_sdwa v[98:99], v72 src0_sel:WORD_1
	v_pk_mul_f32 v[100:101], v[44:45], v[100:101] op_sel:[1,0]
	v_lshlrev_b32_e32 v104, 16, v50
	v_and_b32_e32 v105, 0xffff0000, v50
	v_pk_fma_f32 v[96:97], v[42:43], v[96:97], v[100:101] op_sel:[1,0,0]
	v_pk_mul_f32 v[102:103], v[44:45], v[102:103] op_sel:[1,0]
	s_waitcnt vmcnt(1)
	v_pk_fma_f32 v[96:97], v[26:27], v[96:97], v[104:105]
	v_cvt_pk_f32_fp8_e32 v[104:105], v81
	s_waitcnt vmcnt(0)
	v_cvt_pk_f32_fp8_e32 v[100:101], v74
	v_lshlrev_b32_e32 v106, 16, v51
	v_and_b32_e32 v107, 0xffff0000, v51
	v_pk_fma_f32 v[98:99], v[42:43], v[98:99], v[102:103] op_sel:[1,0,0]
	v_cvt_pk_f32_fp8_sdwa v[102:103], v74 src0_sel:WORD_1
	v_pk_fma_f32 v[98:99], v[28:29], v[98:99], v[106:107]
	v_cvt_pk_f32_fp8_sdwa v[106:107], v81 src0_sel:WORD_1
	v_pk_mul_f32 v[104:105], v[44:45], v[104:105] op_sel:[1,0]
	v_lshlrev_b32_e32 v108, 16, v54
	v_and_b32_e32 v109, 0xffff0000, v54
	v_pk_fma_f32 v[100:101], v[42:43], v[100:101], v[104:105] op_sel:[1,0,0]
	v_pk_mul_f32 v[106:107], v[44:45], v[106:107] op_sel:[1,0]
	v_pk_fma_f32 v[100:101], v[30:31], v[100:101], v[108:109]
	v_pk_add_f32 v[88:89], v[88:89], v[88:89] op_sel:[0,1] op_sel_hi:[1,0]
	v_mul_f32_e32 v63, v100, v100
	v_mul_f32_e32 v104, v101, v101
	v_pk_add_f32 v[94:95], v[94:95], v[94:95] op_sel:[0,1] op_sel_hi:[1,0]
	v_lshlrev_b32_e32 v110, 16, v55
	v_and_b32_e32 v111, 0xffff0000, v55
	v_pk_fma_f32 v[102:103], v[42:43], v[102:103], v[106:107] op_sel:[1,0,0]
	v_mov_b32_e32 v89, v63
	v_mov_b32_e32 v95, v104
	v_pk_fma_f32 v[102:103], v[32:33], v[102:103], v[110:111]
	v_pk_add_f32 v[88:89], v[88:89], v[94:95]
	v_mul_f32_e32 v94, v97, v97
	v_mul_f32_e32 v105, v102, v102
	v_pk_fma_f32 v[94:95], v[96:97], v[96:97], v[94:95] op_sel_hi:[1,1,0]
	v_mul_f32_e32 v104, v99, v99
	v_mul_f32_e32 v106, v103, v103
	v_mov_b32_e32 v95, v105
	v_pk_fma_f32 v[104:105], v[98:99], v[98:99], v[104:105] op_sel_hi:[1,1,0]
	s_nop 0
	v_mov_b32_e32 v105, v106
	v_pk_add_f32 v[94:95], v[94:95], v[104:105]
	s_nop 0
	v_pk_add_f32 v[88:89], v[88:89], v[94:95]
	s_nop 0
	v_add_f32_e32 v63, v88, v89
	v_and_b32_e32 v88, 64, v62
	v_add_u32_e32 v88, 64, v88
	v_xor_b32_e32 v89, 1, v62
	v_cmp_lt_i32_e32 vcc, v89, v88
	s_nop 1
	v_cndmask_b32_e32 v89, v62, v89, vcc
	v_lshlrev_b32_e32 v89, 2, v89
	s_nop 1
	v_add_f32_dpp v237, v63, v63 quad_perm:[1,0,3,2] row_mask:0xf bank_mask:0xf
	s_nop 1
	v_add_f32_dpp v237, v237, v237 quad_perm:[2,3,0,1] row_mask:0xf bank_mask:0xf
	s_nop 1
	v_add_f32_dpp v237, v237, v237 row_half_mirror row_mask:0xf bank_mask:0xf
	s_nop 1
	v_add_f32_dpp v237, v237, v237 row_mirror row_mask:0xf bank_mask:0xf
	s_nop 0
	v_mov_b32_e32 v236, v237
	s_nop 1
	v_permlane16_swap_b32_e32 v237, v236
	s_nop 0
	v_add_f32_e32 v237, v237, v236
	v_mov_b32_e32 v236, v237
	s_nop 1
	v_permlane32_swap_b32_e32 v237, v236
	s_nop 0
	v_add_f32_e32 v237, v237, v236
	s_waitcnt lgkmcnt(0)
	v_xor_b32_e32 v89, 2, v62
	v_cmp_lt_i32_e32 vcc, v89, v88
	s_nop 1
	v_cndmask_b32_e32 v89, v62, v89, vcc
	v_lshlrev_b32_e32 v89, 2, v89
	s_waitcnt lgkmcnt(0)
	v_xor_b32_e32 v89, 4, v62
	v_cmp_lt_i32_e32 vcc, v89, v88
	s_nop 1
	v_cndmask_b32_e32 v89, v62, v89, vcc
	v_lshlrev_b32_e32 v89, 2, v89
	s_waitcnt lgkmcnt(0)
	v_xor_b32_e32 v89, 8, v62
	v_cmp_lt_i32_e32 vcc, v89, v88
	s_nop 1
	v_cndmask_b32_e32 v89, v62, v89, vcc
	v_lshlrev_b32_e32 v89, 2, v89
	s_waitcnt lgkmcnt(0)
	v_xor_b32_e32 v89, 16, v62
	v_cmp_lt_i32_e32 vcc, v89, v88
	s_nop 1
	v_cndmask_b32_e32 v89, v62, v89, vcc
	v_lshlrev_b32_e32 v89, 2, v89
	s_waitcnt lgkmcnt(0)
	v_xor_b32_e32 v89, 32, v62
	v_cmp_lt_i32_e32 vcc, v89, v88
	s_nop 1
	v_cndmask_b32_e32 v62, v62, v89, vcc
	v_lshlrev_b32_e32 v62, 2, v62
	s_waitcnt lgkmcnt(0)
	v_mov_b32_e32 v62, v237
	v_fmamk_f32 v62, v62, 0x3a800000, v68
	v_mul_f32_e32 v63, 0x4b800000, v62
	v_cmp_gt_f32_e32 vcc, s35, v62
	s_nop 1
	v_cndmask_b32_e32 v62, v62, v63, vcc
	v_rsq_f32_e32 v62, v62
	s_nop 0
	v_mul_f32_e32 v63, 0x45800000, v62
	v_cndmask_b32_e32 v88, v62, v63, vcc
	v_pk_mul_f32 v[62:63], v[64:65], v[88:89] op_sel_hi:[1,0]
	v_pk_mul_f32 v[64:65], v[86:87], v[88:89] op_sel_hi:[1,0]
	v_pk_mul_f32 v[62:63], v[2:3], v[62:63]
	v_pk_mul_f32 v[64:65], v[4:5], v[64:65]
	global_store_dwordx4 v[40:41], v[62:65], off
	s_nop 1
	v_pk_mul_f32 v[62:63], v[90:91], v[88:89] op_sel_hi:[1,0]
	v_pk_mul_f32 v[64:65], v[92:93], v[88:89] op_sel_hi:[1,0]
	v_pk_mul_f32 v[62:63], v[6:7], v[62:63]
	v_pk_mul_f32 v[64:65], v[8:9], v[64:65]
	global_store_dwordx4 v[40:41], v[62:65], off offset:1024
	s_nop 1
	v_pk_mul_f32 v[62:63], v[96:97], v[88:89] op_sel_hi:[1,0]
	v_pk_mul_f32 v[64:65], v[98:99], v[88:89] op_sel_hi:[1,0]
	v_pk_mul_f32 v[62:63], v[10:11], v[62:63]
	v_pk_mul_f32 v[64:65], v[12:13], v[64:65]
	global_store_dwordx4 v[40:41], v[62:65], off offset:2048
	s_nop 1
	v_pk_mul_f32 v[62:63], v[100:101], v[88:89] op_sel_hi:[1,0]
	v_pk_mul_f32 v[64:65], v[102:103], v[88:89] op_sel_hi:[1,0]
	v_pk_mul_f32 v[62:63], v[14:15], v[62:63]
	v_pk_mul_f32 v[64:65], v[16:17], v[64:65]
	global_store_dwordx4 v[40:41], v[62:65], off offset:3072
	s_branch .LBB0_2159

.LBB0_2296:
	s_cmp_lt_i32 s74, 19
	s_cselect_b64 s[0:1], -1, 0
	s_and_b64 s[0:1], s[0:1], s[2:3]
	s_andn2_b64 vcc, exec, s[0:1]
	s_cbranch_vccnz .LBB0_2310
	v_readlane_b32 s2, v254, 9
	s_abs_i32 s0, s2
	v_cvt_f32_u32_e32 v0, s0
	s_sub_i32 s3, 0, s0
	s_add_i32 s1, s2, 0x7fff
	s_xor_b32 s2, s1, s2
	v_rcp_iflag_f32_e32 v0, v0
	s_abs_i32 s1, s1
	s_ashr_i32 s2, s2, 31
	v_mul_f32_e32 v0, 0x4f7ffffe, v0
	v_cvt_u32_f32_e32 v0, v0
	s_nop 0
	v_readfirstlane_b32 s4, v0
	s_mul_i32 s3, s3, s4
	s_mul_hi_u32 s3, s4, s3
	s_add_i32 s4, s4, s3
	s_mul_hi_u32 s3, s1, s4
	s_mul_i32 s4, s3, s0
	s_sub_i32 s1, s1, s4
	s_add_i32 s5, s3, 1
	s_sub_i32 s4, s1, s0
	s_cmp_ge_u32 s1, s0
	s_cselect_b32 s3, s5, s3
	s_cselect_b32 s1, s4, s1
	s_add_i32 s4, s3, 1
	s_cmp_ge_u32 s1, s0
	s_cselect_b32 s0, s4, s3
	s_xor_b32 s0, s0, s2
	s_sub_i32 s1, s0, s2
	s_add_i32 s1, s1, 1
	s_and_b32 s0, s1, -2
	s_mul_i32 s2, s0, s97
	s_add_i32 s0, s2, s0
	s_min_i32 s18, s0, 0x8000
	s_cmp_ge_i32 s2, s18
	s_mov_b32 s0, 0
	s_cbranch_scc1 .LBB0_2310
	s_waitcnt vmcnt(0) lgkmcnt(0)
	v_lshlrev_b32_e32 v16, 4, v250
	global_load_dwordx4 v[0:3], v16, s[68:69]
	global_load_dwordx4 v[4:7], v16, s[68:69] offset:1024
	global_load_dwordx4 v[8:11], v16, s[68:69] offset:2048
	global_load_dwordx4 v[12:15], v16, s[68:69] offset:3072
	s_lshl_b32 s19, s31, 14
	s_add_u32 s20, s72, 0x180000
	s_addc_u32 s21, s73, 0
	s_add_u32 s22, s72, 0x140000
	s_addc_u32 s23, s73, 0
	s_cmp_le_i32 s28, s6
	v_lshlrev_b32_e32 v32, 2, v250
	v_mov_b32_e32 v33, 0
	s_cselect_b64 s[4:5], -1, 0
	s_lshr_b32 s1, s1, 1
	v_lshl_add_u64 v[24:25], s[72:73], 0, v[32:33]
	s_mov_b64 s[6:7], 0xdd00000
	s_mul_i32 s1, s1, s97
	s_ashr_i32 s3, s2, 31
	v_lshl_add_u64 v[34:35], v[24:25], 0, s[6:7]
	s_lshl_b32 s6, s1, 2
	s_lshl_b64 s[8:9], s[2:3], 11
	s_add_u32 s8, s72, s8
	v_lshlrev_b32_e32 v24, 3, v250
	v_mov_b32_e32 v25, v33
	s_addc_u32 s9, s73, s9
	v_lshl_add_u64 v[24:25], s[8:9], 0, v[24:25]
	s_mov_b64 s[8:9], 0x8c00e00
	v_lshl_add_u64 v[36:37], v[24:25], 0, s[8:9]
	s_lshl_b64 s[8:9], s[2:3], 12
	s_add_u32 s8, s70, s8
	v_mov_b32_e32 v17, v33
	s_addc_u32 s9, s71, s9
	v_lshl_add_u64 v[16:17], s[8:9], 0, v[16:17]
	s_mov_b64 s[8:9], 0x1000
	v_or_b32_e32 v18, 0x100, v32
	v_or_b32_e32 v20, 0x200, v32
	v_or_b32_e32 v22, 0x300, v32
	v_lshl_add_u64 v[38:39], v[16:17], 0, s[8:9]
	s_mov_b32 s1, s0
	v_mbcnt_lo_u32_b32 v16, -1, 0
	s_mov_b32 s25, -1
	v_mov_b64_e32 v[40:41], s[0:1]
	s_add_i32 s3, 0, 0x20100
	v_lshlrev_b32_e32 v32, 2, v32
	v_lshlrev_b32_e32 v64, 2, v18
	v_lshlrev_b32_e32 v65, 2, v20
	v_lshlrev_b32_e32 v66, 2, v22
	v_mov_b32_e32 v67, 0x358637bd
	s_mov_b32 s24, 0x800000
	s_mov_b64 s[10:11], 0x2000
	v_mbcnt_hi_u32_b32 v68, -1, v16
	v_mov_b64_e32 v[42:43], s[0:1]
	v_mov_b32_e32 v16, 0
	v_mov_b32_e32 v17, v33
	v_mov_b32_e32 v18, v33
	v_mov_b32_e32 v19, v33
	v_mov_b32_e32 v20, v33
	v_mov_b32_e32 v21, v33
	v_mov_b32_e32 v22, v33
	v_mov_b32_e32 v23, v33
	v_mov_b32_e32 v24, v33
	v_mov_b32_e32 v25, v33
	v_mov_b32_e32 v26, v33
	v_mov_b32_e32 v27, v33
	v_mov_b32_e32 v28, v33
	v_mov_b32_e32 v29, v33
	v_mov_b32_e32 v30, v33
	v_mov_b32_e32 v31, v33
	v_lshlrev_b32_e32 v248, 2, v250
	s_ashr_i32 s7, s6, 31
	s_lshl_b64 s[98:99], s[6:7], 2
	s_add_u32 s98, s20, s98
	s_addc_u32 s99, s21, s99
	global_load_dword v249, v248, s[98:99]
	s_mov_b32 s100, 0
	s_waitcnt vmcnt(0)
	s_branch .LBB0_2300

.LBB0_2300:
	s_ashr_i32 s7, s6, 31
	s_lshl_b64 s[0:1], s[6:7], 2
	s_add_u32 s12, s20, s0
	s_addc_u32 s13, s21, s1
	v_readlane_b32 s98, v249, s100
	s_add_i32 s12, s6, 1
	s_ashr_i32 s13, s12, 31
	s_lshl_b64 s[14:15], s[12:13], 2
	s_add_u32 s12, s20, s14
	s_addc_u32 s13, s21, s15
	s_add_i32 s101, s100, 1
	v_readlane_b32 s99, v249, s101
	s_nop 1
	v_mov_b32_e32 v60, s98
	v_mov_b32_e32 v61, s99
	s_waitcnt vmcnt(1)
	v_ashrrev_i32_e32 v62, 15, v60
	v_lshlrev_b32_e32 v62, 2, v62
	v_add_u32_e32 v62, s3, v62
	ds_read_b32 v62, v62
	v_and_b32_e32 v60, 0x7fff, v60
	s_waitcnt vmcnt(0)
	v_ashrrev_i32_e32 v63, 15, v61
	v_lshlrev_b32_e32 v63, 2, v63
	v_add_u32_e32 v63, s3, v63
	ds_read_b32 v63, v63
	s_waitcnt lgkmcnt(1)
	v_lshlrev_b32_e32 v62, 8, v62
	v_add_u32_e32 v62, v62, v60
	v_and_b32_e32 v61, 0x7fff, v61
	s_waitcnt lgkmcnt(0)
	v_lshlrev_b32_e32 v60, 8, v63
	v_add_u32_e32 v60, v60, v61
	v_max_i32_e32 v61, v62, v60
	v_cmp_le_i32_e32 vcc, s19, v61
	s_or_b64 s[12:13], s[4:5], vcc
	s_and_b64 vcc, exec, s[12:13]
	s_cbranch_vccz .LBB0_2302
	s_add_u32 s0, s22, s0
	v_ashrrev_i32_e32 v63, 31, v62
	s_addc_u32 s1, s23, s1
	v_lshlrev_b64 v[50:51], 10, v[62:63]
	v_ashrrev_i32_e32 v61, 31, v60
	s_add_u32 s14, s22, s14
	v_lshl_add_u64 v[62:63], v[34:35], 0, v[50:51]
	v_lshlrev_b64 v[50:51], 10, v[60:61]
	s_addc_u32 s15, s23, s15
	global_load_dword v40, v33, s[0:1]
	global_load_dword v42, v33, s[14:15]
	v_lshl_add_u64 v[60:61], v[34:35], 0, v[50:51]
	global_load_dwordx2 v[50:51], v[36:37], off offset:-3584
	global_load_dwordx2 v[54:55], v[36:37], off offset:-3072
	global_load_dwordx2 v[56:57], v[36:37], off offset:-2560
	global_load_dwordx2 v[58:59], v[36:37], off offset:-2048
	global_load_dword v72, v[62:63], off
	global_load_dword v81, v[60:61], off
	global_load_dword v74, v[62:63], off offset:256
	global_load_dword v82, v[60:61], off offset:256
	global_load_dword v75, v[62:63], off offset:512
	global_load_dword v83, v[60:61], off offset:512
	global_load_dword v84, v[60:61], off offset:768
	global_load_dword v77, v[62:63], off offset:768
	s_waitcnt vmcnt(13)
	v_mul_f32_e32 v40, 0x3d800000, v40
	s_waitcnt vmcnt(12)
	v_mul_f32_e32 v42, 0x3d800000, v42
.LBB0_2302:
	s_add_i32 s0, s6, 2
	s_ashr_i32 s1, s0, 31
	s_lshl_b64 s[14:15], s[0:1], 2
	s_add_u32 s0, s20, s14
	s_addc_u32 s1, s21, s15
	s_add_i32 s101, s100, 2
	v_readlane_b32 s98, v249, s101
	s_add_i32 s0, s6, 3
	s_ashr_i32 s1, s0, 31
	s_lshl_b64 s[16:17], s[0:1], 2
	s_add_u32 s0, s20, s16
	s_addc_u32 s1, s21, s17
	s_add_i32 s101, s100, 3
	v_readlane_b32 s99, v249, s101
	s_nop 1
	v_mov_b32_e32 v60, s98
	v_mov_b32_e32 v61, s99
	s_waitcnt vmcnt(1)
	v_ashrrev_i32_e32 v62, 15, v60
	v_lshlrev_b32_e32 v62, 2, v62
	v_add_u32_e32 v62, s3, v62
	ds_read_b32 v62, v62
	v_and_b32_e32 v60, 0x7fff, v60
	s_waitcnt vmcnt(0)
	v_ashrrev_i32_e32 v63, 15, v61
	v_lshlrev_b32_e32 v63, 2, v63
	v_add_u32_e32 v63, s3, v63
	ds_read_b32 v63, v63
	s_waitcnt lgkmcnt(1)
	v_lshlrev_b32_e32 v62, 8, v62
	v_and_b32_e32 v61, 0x7fff, v61
	v_add_u32_e32 v62, v62, v60
	s_waitcnt lgkmcnt(0)
	v_lshlrev_b32_e32 v60, 8, v63
	v_add_u32_e32 v60, v60, v61
	v_max_i32_e32 v61, v62, v60
	v_cmp_le_i32_e32 vcc, s19, v61
	s_or_b64 s[26:27], s[4:5], vcc
	v_cndmask_b32_e64 v61, 0, 1, s[26:27]
	v_cmp_ne_u32_e64 s[0:1], 1, v61
	s_andn2_b64 vcc, exec, s[26:27]
	s_cbranch_vccnz .LBB0_2304
	s_add_u32 s14, s22, s14
	v_ashrrev_i32_e32 v63, 31, v62
	s_addc_u32 s15, s23, s15
	v_lshlrev_b64 v[44:45], 10, v[62:63]
	v_ashrrev_i32_e32 v61, 31, v60
	s_add_u32 s16, s22, s16
	v_lshl_add_u64 v[62:63], v[34:35], 0, v[44:45]
	v_lshlrev_b64 v[44:45], 10, v[60:61]
	s_addc_u32 s17, s23, s17
	global_load_dword v41, v33, s[14:15]
	global_load_dword v43, v33, s[16:17]
	v_lshl_add_u64 v[60:61], v[34:35], 0, v[44:45]
	global_load_dwordx2 v[44:45], v[36:37], off offset:-1536
	global_load_dwordx2 v[46:47], v[36:37], off offset:-1024
	global_load_dwordx2 v[48:49], v[36:37], off offset:-512
	global_load_dwordx2 v[52:53], v[36:37], off
	global_load_dword v69, v[62:63], off
	global_load_dword v76, v[60:61], off
	global_load_dword v70, v[62:63], off offset:256
	global_load_dword v78, v[60:61], off offset:256
	global_load_dword v71, v[62:63], off offset:512
	global_load_dword v79, v[60:61], off offset:512
	global_load_dword v80, v[60:61], off offset:768
	global_load_dword v73, v[62:63], off offset:768
	s_waitcnt vmcnt(13)
	v_mul_f32_e32 v41, 0x3d800000, v41
	s_waitcnt vmcnt(12)
	v_mul_f32_e32 v43, 0x3d800000, v43

.LBB0_2308:
	v_cvt_pk_f32_fp8_e32 v[86:87], v81
	v_cvt_pk_f32_fp8_sdwa v[88:89], v81 src0_sel:WORD_1
	v_cvt_pk_f32_fp8_e32 v[60:61], v72
	v_cvt_pk_f32_fp8_sdwa v[62:63], v72 src0_sel:WORD_1
	v_pk_mul_f32 v[86:87], v[42:43], v[86:87] op_sel_hi:[0,1]
	v_pk_mul_f32 v[88:89], v[42:43], v[88:89] op_sel_hi:[0,1]
	v_lshlrev_b32_e32 v90, 16, v50
	v_and_b32_e32 v91, 0xffff0000, v50
	v_lshlrev_b32_e32 v92, 16, v51
	v_and_b32_e32 v93, 0xffff0000, v51
	v_pk_fma_f32 v[62:63], v[40:41], v[62:63], v[88:89] op_sel_hi:[0,1,1]
	v_pk_fma_f32 v[60:61], v[40:41], v[60:61], v[86:87] op_sel_hi:[0,1,1]
	s_waitcnt vmcnt(3)
	v_pk_fma_f32 v[60:61], v[16:17], v[60:61], v[90:91]
	v_pk_fma_f32 v[62:63], v[18:19], v[62:63], v[92:93]
	v_pk_mul_f32 v[88:89], v[60:61], v[60:61]
	v_pk_mul_f32 v[86:87], v[62:63], v[62:63]
	v_cvt_pk_f32_fp8_e32 v[92:93], v82
	v_pk_mov_b32 v[90:91], v[88:89], v[86:87] op_sel:[1,0]
	v_mov_b32_e32 v89, v87
	v_cvt_pk_f32_fp8_sdwa v[94:95], v82 src0_sel:WORD_1
	v_pk_add_f32 v[86:87], v[90:91], v[88:89]
	v_cvt_pk_f32_fp8_e32 v[88:89], v74
	v_cvt_pk_f32_fp8_sdwa v[90:91], v74 src0_sel:WORD_1
	v_pk_mul_f32 v[92:93], v[42:43], v[92:93] op_sel_hi:[0,1]
	v_pk_mul_f32 v[94:95], v[42:43], v[94:95] op_sel_hi:[0,1]
	v_lshlrev_b32_e32 v96, 16, v54
	v_and_b32_e32 v97, 0xffff0000, v54
	v_lshlrev_b32_e32 v98, 16, v55
	v_and_b32_e32 v99, 0xffff0000, v55
	v_pk_fma_f32 v[90:91], v[40:41], v[90:91], v[94:95] op_sel_hi:[0,1,1]
	v_pk_fma_f32 v[88:89], v[40:41], v[88:89], v[92:93] op_sel_hi:[0,1,1]
	s_waitcnt vmcnt(2)
	v_pk_fma_f32 v[88:89], v[20:21], v[88:89], v[96:97]
	v_pk_fma_f32 v[90:91], v[22:23], v[90:91], v[98:99]
	v_pk_mul_f32 v[94:95], v[88:89], v[88:89]
	v_pk_mul_f32 v[92:93], v[90:91], v[90:91]
	v_cvt_pk_f32_fp8_e32 v[98:99], v83
	v_pk_mov_b32 v[96:97], v[94:95], v[92:93] op_sel:[1,0]
	v_mov_b32_e32 v95, v93
	v_pk_add_f32 v[92:93], v[96:97], v[94:95]
	v_cvt_pk_f32_fp8_e32 v[94:95], v75
	v_cvt_pk_f32_fp8_sdwa v[100:101], v83 src0_sel:WORD_1
	v_cvt_pk_f32_fp8_sdwa v[96:97], v75 src0_sel:WORD_1
	v_pk_mul_f32 v[98:99], v[42:43], v[98:99] op_sel_hi:[0,1]
	v_lshlrev_b32_e32 v102, 16, v56
	v_and_b32_e32 v103, 0xffff0000, v56
	v_pk_fma_f32 v[94:95], v[40:41], v[94:95], v[98:99] op_sel_hi:[0,1,1]
	s_waitcnt vmcnt(1)
	v_pk_fma_f32 v[94:95], v[24:25], v[94:95], v[102:103]
	v_cvt_pk_f32_fp8_e32 v[102:103], v84
	v_pk_mul_f32 v[100:101], v[42:43], v[100:101] op_sel_hi:[0,1]
	v_cvt_pk_f32_fp8_e32 v[98:99], v77
	v_lshlrev_b32_e32 v104, 16, v57
	v_and_b32_e32 v105, 0xffff0000, v57
	v_pk_fma_f32 v[96:97], v[40:41], v[96:97], v[100:101] op_sel_hi:[0,1,1]
	v_pk_fma_f32 v[96:97], v[26:27], v[96:97], v[104:105]
	v_cvt_pk_f32_fp8_sdwa v[104:105], v84 src0_sel:WORD_1
	v_cvt_pk_f32_fp8_sdwa v[100:101], v77 src0_sel:WORD_1
	v_pk_mul_f32 v[102:103], v[42:43], v[102:103] op_sel_hi:[0,1]
	v_lshlrev_b32_e32 v106, 16, v58
	v_and_b32_e32 v107, 0xffff0000, v58
	v_pk_fma_f32 v[98:99], v[40:41], v[98:99], v[102:103] op_sel_hi:[0,1,1]
	s_waitcnt vmcnt(0)
	v_pk_fma_f32 v[98:99], v[28:29], v[98:99], v[106:107]
	v_pk_mul_f32 v[104:105], v[42:43], v[104:105] op_sel_hi:[0,1]
	v_mul_f32_e32 v85, v98, v98
	v_mul_f32_e32 v102, v99, v99
	v_pk_add_f32 v[86:87], v[86:87], v[86:87] op_sel:[0,1] op_sel_hi:[1,0]
	v_pk_add_f32 v[92:93], v[92:93], v[92:93] op_sel:[0,1] op_sel_hi:[1,0]
	v_lshlrev_b32_e32 v108, 16, v59
	v_and_b32_e32 v109, 0xffff0000, v59
	v_pk_fma_f32 v[100:101], v[40:41], v[100:101], v[104:105] op_sel_hi:[0,1,1]
	v_mov_b32_e32 v87, v85
	v_mov_b32_e32 v93, v102
	v_pk_fma_f32 v[100:101], v[30:31], v[100:101], v[108:109]
	v_pk_add_f32 v[86:87], v[86:87], v[92:93]
	v_mul_f32_e32 v92, v95, v95
	v_mul_f32_e32 v103, v100, v100
	v_pk_fma_f32 v[92:93], v[94:95], v[94:95], v[92:93] op_sel_hi:[1,1,0]
	v_mul_f32_e32 v102, v97, v97
	v_mul_f32_e32 v104, v101, v101
	v_mov_b32_e32 v93, v103
	v_pk_fma_f32 v[102:103], v[96:97], v[96:97], v[102:103] op_sel_hi:[1,1,0]
	s_nop 0
	v_mov_b32_e32 v103, v104
	v_pk_add_f32 v[92:93], v[92:93], v[102:103]
	s_nop 0
	v_pk_add_f32 v[86:87], v[86:87], v[92:93]
	s_nop 0
	v_add_f32_e32 v85, v86, v87
	v_and_b32_e32 v86, 64, v68
	v_add_u32_e32 v86, 64, v86
	v_xor_b32_e32 v87, 1, v68
	v_cmp_lt_i32_e32 vcc, v87, v86
	s_nop 1
	v_cndmask_b32_e32 v87, v68, v87, vcc
	v_lshlrev_b32_e32 v87, 2, v87
	s_nop 1
	v_add_f32_dpp v237, v85, v85 quad_perm:[1,0,3,2] row_mask:0xf bank_mask:0xf
	s_nop 1
	v_add_f32_dpp v237, v237, v237 quad_perm:[2,3,0,1] row_mask:0xf bank_mask:0xf
	s_nop 1
	v_add_f32_dpp v237, v237, v237 row_half_mirror row_mask:0xf bank_mask:0xf
	s_nop 1
	v_add_f32_dpp v237, v237, v237 row_mirror row_mask:0xf bank_mask:0xf
	s_nop 0
	v_mov_b32_e32 v236, v237
	s_nop 1
	v_permlane16_swap_b32_e32 v237, v236
	s_nop 0
	v_add_f32_e32 v237, v237, v236
	v_mov_b32_e32 v236, v237
	s_nop 1
	v_permlane32_swap_b32_e32 v237, v236
	s_nop 0
	v_add_f32_e32 v237, v237, v236
	s_waitcnt lgkmcnt(0)
	v_xor_b32_e32 v87, 2, v68
	v_cmp_lt_i32_e32 vcc, v87, v86
	s_nop 1
	v_cndmask_b32_e32 v87, v68, v87, vcc
	v_lshlrev_b32_e32 v87, 2, v87
	s_waitcnt lgkmcnt(0)
	v_xor_b32_e32 v87, 4, v68
	v_cmp_lt_i32_e32 vcc, v87, v86
	s_nop 1
	v_cndmask_b32_e32 v87, v68, v87, vcc
	v_lshlrev_b32_e32 v87, 2, v87
	s_waitcnt lgkmcnt(0)
	v_xor_b32_e32 v87, 8, v68
	v_cmp_lt_i32_e32 vcc, v87, v86
	s_nop 1
	v_cndmask_b32_e32 v87, v68, v87, vcc
	v_lshlrev_b32_e32 v87, 2, v87
	s_waitcnt lgkmcnt(0)
	v_xor_b32_e32 v87, 16, v68
	v_cmp_lt_i32_e32 vcc, v87, v86
	s_nop 1
	v_cndmask_b32_e32 v87, v68, v87, vcc
	v_lshlrev_b32_e32 v87, 2, v87
	s_waitcnt lgkmcnt(0)
	v_xor_b32_e32 v87, 32, v68
	v_cmp_lt_i32_e32 vcc, v87, v86
	s_nop 1
	v_cndmask_b32_e32 v86, v68, v87, vcc
	v_lshlrev_b32_e32 v86, 2, v86
	s_waitcnt lgkmcnt(0)
	v_mov_b32_e32 v85, v237
	v_fmamk_f32 v85, v85, 0x3a800000, v67
	v_mul_f32_e32 v86, 0x4b800000, v85
	v_cmp_gt_f32_e32 vcc, s24, v85
	s_nop 1
	v_cndmask_b32_e32 v85, v85, v86, vcc
	v_rsq_f32_e32 v85, v85
	s_nop 0
	v_mul_f32_e32 v86, 0x45800000, v85
	v_cndmask_b32_e32 v86, v85, v86, vcc
	v_pk_mul_f32 v[60:61], v[60:61], v[86:87] op_sel_hi:[1,0]
	v_pk_mul_f32 v[62:63], v[62:63], v[86:87] op_sel_hi:[1,0]
	v_pk_mul_f32 v[60:61], v[0:1], v[60:61]
	v_pk_mul_f32 v[62:63], v[2:3], v[62:63]
	global_store_dwordx4 v[38:39], v[60:63], off offset:-4096
	s_nop 1
	v_pk_mul_f32 v[60:61], v[88:89], v[86:87] op_sel_hi:[1,0]
	v_pk_mul_f32 v[62:63], v[90:91], v[86:87] op_sel_hi:[1,0]
	v_pk_mul_f32 v[60:61], v[4:5], v[60:61]
	v_pk_mul_f32 v[62:63], v[6:7], v[62:63]
	global_store_dwordx4 v[38:39], v[60:63], off offset:-3072
	s_nop 1
	v_pk_mul_f32 v[60:61], v[94:95], v[86:87] op_sel_hi:[1,0]
	v_pk_mul_f32 v[62:63], v[96:97], v[86:87] op_sel_hi:[1,0]
	v_pk_mul_f32 v[60:61], v[8:9], v[60:61]
	v_pk_mul_f32 v[62:63], v[10:11], v[62:63]
	global_store_dwordx4 v[38:39], v[60:63], off offset:-2048
	s_nop 1
	v_pk_mul_f32 v[60:61], v[98:99], v[86:87] op_sel_hi:[1,0]
	v_pk_mul_f32 v[62:63], v[100:101], v[86:87] op_sel_hi:[1,0]
	v_pk_mul_f32 v[60:61], v[12:13], v[60:61]
	v_pk_mul_f32 v[62:63], v[14:15], v[62:63]
	global_store_dwordx4 v[38:39], v[60:63], off offset:-1024
	s_and_b64 vcc, exec, s[0:1]
	s_cbranch_vccnz .LBB0_2299
.LBB0_2309:
	s_waitcnt vmcnt(6)
	v_cvt_pk_f32_fp8_e32 v[86:87], v76
	v_cvt_pk_f32_fp8_sdwa v[88:89], v76 src0_sel:WORD_1
	v_cvt_pk_f32_fp8_e32 v[60:61], v69
	v_cvt_pk_f32_fp8_sdwa v[62:63], v69 src0_sel:WORD_1
	v_pk_mul_f32 v[86:87], v[42:43], v[86:87] op_sel:[1,0]
	v_pk_mul_f32 v[88:89], v[42:43], v[88:89] op_sel:[1,0]
	v_lshlrev_b32_e32 v90, 16, v44
	v_and_b32_e32 v91, 0xffff0000, v44
	v_lshlrev_b32_e32 v92, 16, v45
	v_and_b32_e32 v93, 0xffff0000, v45
	v_pk_fma_f32 v[62:63], v[40:41], v[62:63], v[88:89] op_sel:[1,0,0]
	v_pk_fma_f32 v[60:61], v[40:41], v[60:61], v[86:87] op_sel:[1,0,0]
	s_waitcnt vmcnt(3)
	v_pk_fma_f32 v[62:63], v[18:19], v[62:63], v[92:93]
	v_pk_fma_f32 v[60:61], v[16:17], v[60:61], v[90:91]
	v_pk_mul_f32 v[86:87], v[62:63], v[62:63]
	v_pk_mul_f32 v[88:89], v[60:61], v[60:61]
	v_cvt_pk_f32_fp8_e32 v[92:93], v78
	v_pk_mov_b32 v[90:91], v[88:89], v[86:87] op_sel:[1,0]
	v_mov_b32_e32 v89, v87
	v_cvt_pk_f32_fp8_sdwa v[94:95], v78 src0_sel:WORD_1
	v_pk_add_f32 v[86:87], v[90:91], v[88:89]
	v_cvt_pk_f32_fp8_e32 v[88:89], v70
	v_cvt_pk_f32_fp8_sdwa v[90:91], v70 src0_sel:WORD_1
	v_pk_mul_f32 v[92:93], v[42:43], v[92:93] op_sel:[1,0]
	v_pk_mul_f32 v[94:95], v[42:43], v[94:95] op_sel:[1,0]
	v_lshlrev_b32_e32 v96, 16, v46
	v_and_b32_e32 v97, 0xffff0000, v46
	v_lshlrev_b32_e32 v98, 16, v47
	v_and_b32_e32 v99, 0xffff0000, v47
	v_pk_fma_f32 v[90:91], v[40:41], v[90:91], v[94:95] op_sel:[1,0,0]
	v_pk_fma_f32 v[88:89], v[40:41], v[88:89], v[92:93] op_sel:[1,0,0]
	s_waitcnt vmcnt(2)
	v_pk_fma_f32 v[90:91], v[22:23], v[90:91], v[98:99]
	v_pk_fma_f32 v[88:89], v[20:21], v[88:89], v[96:97]
	v_pk_mul_f32 v[92:93], v[90:91], v[90:91]
	v_pk_mul_f32 v[94:95], v[88:89], v[88:89]
	v_cvt_pk_f32_fp8_e32 v[98:99], v79
	v_pk_mov_b32 v[96:97], v[94:95], v[92:93] op_sel:[1,0]
	v_mov_b32_e32 v95, v93
	v_pk_add_f32 v[92:93], v[96:97], v[94:95]
	v_cvt_pk_f32_fp8_e32 v[94:95], v71
	v_cvt_pk_f32_fp8_sdwa v[100:101], v79 src0_sel:WORD_1
	v_cvt_pk_f32_fp8_sdwa v[96:97], v71 src0_sel:WORD_1
	v_pk_mul_f32 v[98:99], v[42:43], v[98:99] op_sel:[1,0]
	v_lshlrev_b32_e32 v102, 16, v48
	v_and_b32_e32 v103, 0xffff0000, v48
	v_pk_fma_f32 v[94:95], v[40:41], v[94:95], v[98:99] op_sel:[1,0,0]
	v_pk_mul_f32 v[100:101], v[42:43], v[100:101] op_sel:[1,0]
	s_waitcnt vmcnt(1)
	v_pk_fma_f32 v[94:95], v[24:25], v[94:95], v[102:103]
	v_cvt_pk_f32_fp8_e32 v[102:103], v80
	s_waitcnt vmcnt(0)
	v_cvt_pk_f32_fp8_e32 v[98:99], v73
	v_lshlrev_b32_e32 v104, 16, v49
	v_and_b32_e32 v105, 0xffff0000, v49
	v_pk_fma_f32 v[96:97], v[40:41], v[96:97], v[100:101] op_sel:[1,0,0]
	v_cvt_pk_f32_fp8_sdwa v[100:101], v73 src0_sel:WORD_1
	v_pk_fma_f32 v[96:97], v[26:27], v[96:97], v[104:105]
	v_cvt_pk_f32_fp8_sdwa v[104:105], v80 src0_sel:WORD_1
	v_pk_mul_f32 v[102:103], v[42:43], v[102:103] op_sel:[1,0]
	v_lshlrev_b32_e32 v106, 16, v52
	v_and_b32_e32 v107, 0xffff0000, v52
	v_pk_fma_f32 v[98:99], v[40:41], v[98:99], v[102:103] op_sel:[1,0,0]
	v_pk_mul_f32 v[104:105], v[42:43], v[104:105] op_sel:[1,0]
	v_pk_fma_f32 v[98:99], v[28:29], v[98:99], v[106:107]
	v_pk_add_f32 v[86:87], v[86:87], v[86:87] op_sel:[0,1] op_sel_hi:[1,0]
	v_mul_f32_e32 v85, v98, v98
	v_mul_f32_e32 v102, v99, v99
	v_pk_add_f32 v[92:93], v[92:93], v[92:93] op_sel:[0,1] op_sel_hi:[1,0]
	v_lshlrev_b32_e32 v108, 16, v53
	v_and_b32_e32 v109, 0xffff0000, v53
	v_pk_fma_f32 v[100:101], v[40:41], v[100:101], v[104:105] op_sel:[1,0,0]
	v_mov_b32_e32 v87, v85
	v_mov_b32_e32 v93, v102
	v_pk_fma_f32 v[100:101], v[30:31], v[100:101], v[108:109]
	v_pk_add_f32 v[86:87], v[86:87], v[92:93]
	v_mul_f32_e32 v92, v95, v95
	v_mul_f32_e32 v103, v100, v100
	v_pk_fma_f32 v[92:93], v[94:95], v[94:95], v[92:93] op_sel_hi:[1,1,0]
	v_mul_f32_e32 v102, v97, v97
	v_mul_f32_e32 v104, v101, v101
	v_mov_b32_e32 v93, v103
	v_pk_fma_f32 v[102:103], v[96:97], v[96:97], v[102:103] op_sel_hi:[1,1,0]
	s_nop 0
	v_mov_b32_e32 v103, v104
	v_pk_add_f32 v[92:93], v[92:93], v[102:103]
	s_nop 0
	v_pk_add_f32 v[86:87], v[86:87], v[92:93]
	s_nop 0
	v_add_f32_e32 v85, v86, v87
	v_and_b32_e32 v86, 64, v68
	v_add_u32_e32 v86, 64, v86
	v_xor_b32_e32 v87, 1, v68
	v_cmp_lt_i32_e32 vcc, v87, v86
	s_nop 1
	v_cndmask_b32_e32 v87, v68, v87, vcc
	v_lshlrev_b32_e32 v87, 2, v87
	s_nop 1
	v_add_f32_dpp v237, v85, v85 quad_perm:[1,0,3,2] row_mask:0xf bank_mask:0xf
	s_nop 1
	v_add_f32_dpp v237, v237, v237 quad_perm:[2,3,0,1] row_mask:0xf bank_mask:0xf
	s_nop 1
	v_add_f32_dpp v237, v237, v237 row_half_mirror row_mask:0xf bank_mask:0xf
	s_nop 1
	v_add_f32_dpp v237, v237, v237 row_mirror row_mask:0xf bank_mask:0xf
	s_nop 0
	v_mov_b32_e32 v236, v237
	s_nop 1
	v_permlane16_swap_b32_e32 v237, v236
	s_nop 0
	v_add_f32_e32 v237, v237, v236
	v_mov_b32_e32 v236, v237
	s_nop 1
	v_permlane32_swap_b32_e32 v237, v236
	s_nop 0
	v_add_f32_e32 v237, v237, v236
	s_waitcnt lgkmcnt(0)
	v_xor_b32_e32 v87, 2, v68
	v_cmp_lt_i32_e32 vcc, v87, v86
	s_nop 1
	v_cndmask_b32_e32 v87, v68, v87, vcc
	v_lshlrev_b32_e32 v87, 2, v87
	s_waitcnt lgkmcnt(0)
	v_xor_b32_e32 v87, 4, v68
	v_cmp_lt_i32_e32 vcc, v87, v86
	s_nop 1
	v_cndmask_b32_e32 v87, v68, v87, vcc
	v_lshlrev_b32_e32 v87, 2, v87
	s_waitcnt lgkmcnt(0)
	v_xor_b32_e32 v87, 8, v68
	v_cmp_lt_i32_e32 vcc, v87, v86
	s_nop 1
	v_cndmask_b32_e32 v87, v68, v87, vcc
	v_lshlrev_b32_e32 v87, 2, v87
	s_waitcnt lgkmcnt(0)
	v_xor_b32_e32 v87, 16, v68
	v_cmp_lt_i32_e32 vcc, v87, v86
	s_nop 1
	v_cndmask_b32_e32 v87, v68, v87, vcc
	v_lshlrev_b32_e32 v87, 2, v87
	s_waitcnt lgkmcnt(0)
	v_xor_b32_e32 v87, 32, v68
	v_cmp_lt_i32_e32 vcc, v87, v86
	s_nop 1
	v_cndmask_b32_e32 v86, v68, v87, vcc
	v_lshlrev_b32_e32 v86, 2, v86
	s_waitcnt lgkmcnt(0)
	v_mov_b32_e32 v85, v237
	v_fmamk_f32 v85, v85, 0x3a800000, v67
	v_mul_f32_e32 v86, 0x4b800000, v85
	v_cmp_gt_f32_e32 vcc, s24, v85
	s_nop 1
	v_cndmask_b32_e32 v85, v85, v86, vcc
	v_rsq_f32_e32 v85, v85
	s_nop 0
	v_mul_f32_e32 v86, 0x45800000, v85
	v_cndmask_b32_e32 v86, v85, v86, vcc
	v_pk_mul_f32 v[60:61], v[60:61], v[86:87] op_sel_hi:[1,0]
	v_pk_mul_f32 v[62:63], v[62:63], v[86:87] op_sel_hi:[1,0]
	v_pk_mul_f32 v[60:61], v[0:1], v[60:61]
	v_pk_mul_f32 v[62:63], v[2:3], v[62:63]
	global_store_dwordx4 v[38:39], v[60:63], off
	s_nop 1
	v_pk_mul_f32 v[60:61], v[88:89], v[86:87] op_sel_hi:[1,0]
	v_pk_mul_f32 v[62:63], v[90:91], v[86:87] op_sel_hi:[1,0]
	v_pk_mul_f32 v[60:61], v[4:5], v[60:61]
	v_pk_mul_f32 v[62:63], v[6:7], v[62:63]
	global_store_dwordx4 v[38:39], v[60:63], off offset:1024
	s_nop 1
	v_pk_mul_f32 v[60:61], v[94:95], v[86:87] op_sel_hi:[1,0]
	v_pk_mul_f32 v[62:63], v[96:97], v[86:87] op_sel_hi:[1,0]
	v_pk_mul_f32 v[60:61], v[8:9], v[60:61]
	v_pk_mul_f32 v[62:63], v[10:11], v[62:63]
	global_store_dwordx4 v[38:39], v[60:63], off offset:2048
	s_nop 1
	v_pk_mul_f32 v[60:61], v[98:99], v[86:87] op_sel_hi:[1,0]
	v_pk_mul_f32 v[62:63], v[100:101], v[86:87] op_sel_hi:[1,0]
	v_pk_mul_f32 v[60:61], v[12:13], v[60:61]
	v_pk_mul_f32 v[62:63], v[14:15], v[62:63]
	global_store_dwordx4 v[38:39], v[60:63], off offset:3072
	s_branch .LBB0_2299
